# removed the redundant s_setprio 0 / s_setprio 3 pair in the middle of every K-loop MFMA block
# speedup vs baseline: 1.0270x; 1.0035x over previous
.LBB0_252:
	ds_read_b128 v[40:43], v161
	ds_read_b128 v[44:47], v161 offset:1024
	ds_read_b128 v[56:59], v161 offset:2048
	ds_read_b128 v[60:63], v161 offset:3072
	ds_read_b128 v[148:151], v162
	ds_read_b128 v[152:155], v162 offset:1024
	ds_read_b128 v[164:167], v162 offset:2048
	ds_read_b128 v[168:171], v162 offset:3072
	s_add_u32 s25, s30, 0xfffa0080
	s_addc_u32 s34, s31, -1
	s_cmp_eq_u32 s23, 12
	s_cselect_b32 s35, s27, s34
	s_cselect_b32 s34, s26, s25
	s_cselect_b32 s40, s28, s5
	s_cselect_b32 s41, s29, s18
	s_add_u32 s38, s34, 0x80
	s_addc_u32 s39, s35, 0
	s_add_u32 s78, s30, 0xfffe0000
	v_mov_b32_e32 v146, v159
	s_addc_u32 s79, s31, -1
	ds_read_b128 v[172:175], v163
	ds_read_b128 v[176:179], v163 offset:1024
	ds_read_b128 v[180:183], v163 offset:2048
	ds_read_b128 v[184:187], v163 offset:3072
	ds_read_b128 v[188:191], v163 offset:4096
	ds_read_b128 v[192:195], v163 offset:5120
	ds_read_b128 v[196:199], v163 offset:6144
	ds_read_b128 v[200:203], v163 offset:7168
	s_add_i32 m0, s52, 0xc000
	s_nop 0
	global_load_lds_dwordx4 v146, s[78:79]
	v_mov_b32_e32 v146, v159
	s_mov_b64 s[78:79], s[30:31]
	s_add_i32 m0, s52, 0xe000
	s_nop 0
	global_load_lds_dwordx4 v146, s[78:79]
	s_waitcnt vmcnt(8)
	s_waitcnt lgkmcnt(0)
	s_barrier
	s_setprio 3
	s_waitcnt lgkmcnt(0)
	v_mfma_f32_16x16x32_bf16 v[140:143], v[40:43], v[172:175], v[140:143]
	v_mfma_f32_16x16x32_bf16 v[132:135], v[56:59], v[172:175], v[132:135]
	v_mfma_f32_16x16x32_bf16 v[124:127], v[40:43], v[180:183], v[124:127]
	v_mfma_f32_16x16x32_bf16 v[116:119], v[56:59], v[180:183], v[116:119]
	v_mfma_f32_16x16x32_bf16 v[108:111], v[40:43], v[188:191], v[108:111]
	v_mfma_f32_16x16x32_bf16 v[100:103], v[56:59], v[188:191], v[100:103]
	v_mfma_f32_16x16x32_bf16 v[92:95], v[40:43], v[196:199], v[92:95]
	v_mfma_f32_16x16x32_bf16 v[84:87], v[56:59], v[196:199], v[84:87]
	v_mfma_f32_16x16x32_bf16 v[140:143], v[44:47], v[176:179], v[140:143]
	v_mfma_f32_16x16x32_bf16 v[132:135], v[60:63], v[176:179], v[132:135]
	v_mfma_f32_16x16x32_bf16 v[124:127], v[44:47], v[184:187], v[124:127]
	v_mfma_f32_16x16x32_bf16 v[116:119], v[60:63], v[184:187], v[116:119]
	v_mfma_f32_16x16x32_bf16 v[108:111], v[44:47], v[192:195], v[108:111]
	v_mfma_f32_16x16x32_bf16 v[100:103], v[60:63], v[192:195], v[100:103]
	v_mfma_f32_16x16x32_bf16 v[92:95], v[44:47], v[200:203], v[92:95]
	v_mfma_f32_16x16x32_bf16 v[84:87], v[60:63], v[200:203], v[84:87]
	v_mfma_f32_16x16x32_bf16 v[136:139], v[148:151], v[172:175], v[136:139]
	v_mfma_f32_16x16x32_bf16 v[128:131], v[164:167], v[172:175], v[128:131]
	v_mfma_f32_16x16x32_bf16 v[120:123], v[148:151], v[180:183], v[120:123]
	v_mfma_f32_16x16x32_bf16 v[112:115], v[164:167], v[180:183], v[112:115]
	v_mfma_f32_16x16x32_bf16 v[104:107], v[148:151], v[188:191], v[104:107]
	v_mfma_f32_16x16x32_bf16 v[96:99], v[164:167], v[188:191], v[96:99]
	v_mfma_f32_16x16x32_bf16 v[88:91], v[148:151], v[196:199], v[88:91]
	v_mfma_f32_16x16x32_bf16 v[80:83], v[164:167], v[196:199], v[80:83]
	v_mfma_f32_16x16x32_bf16 v[136:139], v[152:155], v[176:179], v[136:139]
	v_mfma_f32_16x16x32_bf16 v[128:131], v[168:171], v[176:179], v[128:131]
	v_mfma_f32_16x16x32_bf16 v[120:123], v[152:155], v[184:187], v[120:123]
	v_mfma_f32_16x16x32_bf16 v[112:115], v[168:171], v[184:187], v[112:115]
	v_mfma_f32_16x16x32_bf16 v[104:107], v[152:155], v[192:195], v[104:107]
	v_mfma_f32_16x16x32_bf16 v[96:99], v[168:171], v[192:195], v[96:99]
	v_mfma_f32_16x16x32_bf16 v[88:91], v[152:155], v[200:203], v[88:91]
	v_mfma_f32_16x16x32_bf16 v[80:83], v[168:171], v[200:203], v[80:83]
	s_setprio 0
	s_barrier
	v_mov_b32_e32 v146, v158
	s_mov_b64 s[78:79], s[40:41]
	s_add_i32 s25, s72, s51
	ds_read_b128 v[172:175], v163 offset:16384
	ds_read_b128 v[176:179], v163 offset:17408
	ds_read_b128 v[180:183], v163 offset:18432
	ds_read_b128 v[184:187], v163 offset:19456
	ds_read_b128 v[188:191], v163 offset:20480
	ds_read_b128 v[192:195], v163 offset:21504
	ds_read_b128 v[196:199], v163 offset:22528
	ds_read_b128 v[200:203], v163 offset:23552
	s_mov_b32 m0, s25
	s_nop 0
	global_load_lds_dwordx4 v146, s[78:79]
	s_add_u32 s78, s40, 0x20000
	v_mov_b32_e32 v146, v158
	s_addc_u32 s79, s41, 0
	s_add_i32 m0, s25, 0x2000
	s_nop 0
	global_load_lds_dwordx4 v146, s[78:79]
	s_add_u32 s78, s40, 0x40000
	v_mov_b32_e32 v146, v158
	s_addc_u32 s79, s41, 0
	s_add_i32 s25, s73, s51
	s_mov_b32 m0, s25
	s_nop 0
	global_load_lds_dwordx4 v146, s[78:79]
	s_add_u32 s78, s40, 0x60000
	v_mov_b32_e32 v146, v158
	s_addc_u32 s79, s41, 0
	s_add_i32 m0, s25, 0x2000
	s_nop 0
	global_load_lds_dwordx4 v146, s[78:79]
	v_mov_b32_e32 v146, v159
	s_mov_b64 s[78:79], s[34:35]
	s_mov_b32 m0, s52
	s_nop 0
	global_load_lds_dwordx4 v146, s[78:79]
	s_add_u32 s78, s34, 0x20000
	v_mov_b32_e32 v146, v159
	s_addc_u32 s79, s35, 0
	s_mov_b32 m0, s53
	s_nop 0
	global_load_lds_dwordx4 v146, s[78:79]
	s_waitcnt vmcnt(8)
	s_waitcnt lgkmcnt(0)
	s_barrier
	s_setprio 3
	s_waitcnt lgkmcnt(0)
	v_mfma_f32_16x16x32_bf16 v[76:79], v[40:43], v[172:175], v[76:79]
	v_mfma_f32_16x16x32_bf16 v[68:71], v[56:59], v[172:175], v[68:71]
	v_mfma_f32_16x16x32_bf16 v[52:55], v[40:43], v[180:183], v[52:55]
	v_mfma_f32_16x16x32_bf16 v[36:39], v[56:59], v[180:183], v[36:39]
	v_mfma_f32_16x16x32_bf16 v[28:31], v[40:43], v[188:191], v[28:31]
	v_mfma_f32_16x16x32_bf16 v[20:23], v[56:59], v[188:191], v[20:23]
	v_mfma_f32_16x16x32_bf16 v[12:15], v[40:43], v[196:199], v[12:15]
	v_mfma_f32_16x16x32_bf16 v[4:7], v[56:59], v[196:199], v[4:7]
	v_mfma_f32_16x16x32_bf16 v[76:79], v[44:47], v[176:179], v[76:79]
	v_mfma_f32_16x16x32_bf16 v[68:71], v[60:63], v[176:179], v[68:71]
	v_mfma_f32_16x16x32_bf16 v[52:55], v[44:47], v[184:187], v[52:55]
	v_mfma_f32_16x16x32_bf16 v[36:39], v[60:63], v[184:187], v[36:39]
	v_mfma_f32_16x16x32_bf16 v[28:31], v[44:47], v[192:195], v[28:31]
	v_mfma_f32_16x16x32_bf16 v[20:23], v[60:63], v[192:195], v[20:23]
	v_mfma_f32_16x16x32_bf16 v[12:15], v[44:47], v[200:203], v[12:15]
	v_mfma_f32_16x16x32_bf16 v[4:7], v[60:63], v[200:203], v[4:7]
	v_mfma_f32_16x16x32_bf16 v[48:51], v[148:151], v[180:183], v[48:51]
	v_mfma_f32_16x16x32_bf16 v[32:35], v[164:167], v[180:183], v[32:35]
	v_mfma_f32_16x16x32_bf16 v[24:27], v[148:151], v[188:191], v[24:27]
	v_mfma_f32_16x16x32_bf16 v[16:19], v[164:167], v[188:191], v[16:19]
	v_mfma_f32_16x16x32_bf16 v[8:11], v[148:151], v[196:199], v[8:11]
	v_mfma_f32_16x16x32_bf16 v[0:3], v[164:167], v[196:199], v[0:3]
	v_mfma_f32_16x16x32_bf16 v[40:43], v[148:151], v[172:175], v[72:75]
	v_mfma_f32_16x16x32_bf16 v[44:47], v[164:167], v[172:175], v[64:67]
	v_mfma_f32_16x16x32_bf16 v[48:51], v[152:155], v[184:187], v[48:51]
	v_mfma_f32_16x16x32_bf16 v[32:35], v[168:171], v[184:187], v[32:35]
	v_mfma_f32_16x16x32_bf16 v[24:27], v[152:155], v[192:195], v[24:27]
	v_mfma_f32_16x16x32_bf16 v[16:19], v[168:171], v[192:195], v[16:19]
	v_mfma_f32_16x16x32_bf16 v[8:11], v[152:155], v[200:203], v[8:11]
	v_mfma_f32_16x16x32_bf16 v[0:3], v[168:171], v[200:203], v[0:3]
	v_mfma_f32_16x16x32_bf16 v[40:43], v[152:155], v[176:179], v[40:43]
	v_mfma_f32_16x16x32_bf16 v[44:47], v[168:171], v[176:179], v[44:47]
	s_setprio 0
	s_barrier
	s_add_i32 s25, 0, 0x18000
	s_add_i32 s37, 0, 0x1c000
	v_add_u32_e32 v72, s25, v160
	v_add_u32_e32 v146, s37, v160
	ds_read_b128 v[56:59], v72
	ds_read_b128 v[60:63], v72 offset:1024
	ds_read_b128 v[64:67], v72 offset:2048
	ds_read_b128 v[72:75], v72 offset:3072
	ds_read_b128 v[148:151], v146
	ds_read_b128 v[152:155], v146 offset:1024
	ds_read_b128 v[164:167], v146 offset:2048
	ds_read_b128 v[168:171], v146 offset:3072
	s_add_u32 s78, s34, 0x40000
	v_mov_b32_e32 v146, v159
	s_addc_u32 s79, s35, 0
	s_mov_b32 m0, s60
	ds_read_b128 v[172:175], v163 offset:32768
	ds_read_b128 v[176:179], v163 offset:33792
	ds_read_b128 v[180:183], v163 offset:34816
	ds_read_b128 v[184:187], v163 offset:35840
	ds_read_b128 v[188:191], v163 offset:36864
	ds_read_b128 v[192:195], v163 offset:37888
	ds_read_b128 v[196:199], v163 offset:38912
	ds_read_b128 v[200:203], v163 offset:39936
	s_nop 0
	global_load_lds_dwordx4 v146, s[78:79]
	s_add_u32 s78, s34, 0x60000
	v_mov_b32_e32 v146, v159
	s_addc_u32 s79, s35, 0
	s_mov_b32 m0, s61
	s_nop 0
	global_load_lds_dwordx4 v146, s[78:79]
	s_waitcnt vmcnt(8)
	s_waitcnt lgkmcnt(0)
	s_barrier
	s_setprio 3
	s_waitcnt lgkmcnt(0)
	v_mfma_f32_16x16x32_bf16 v[140:143], v[56:59], v[172:175], v[140:143]
	v_mfma_f32_16x16x32_bf16 v[132:135], v[64:67], v[172:175], v[132:135]
	v_mfma_f32_16x16x32_bf16 v[124:127], v[56:59], v[180:183], v[124:127]
	v_mfma_f32_16x16x32_bf16 v[116:119], v[64:67], v[180:183], v[116:119]
	v_mfma_f32_16x16x32_bf16 v[108:111], v[56:59], v[188:191], v[108:111]
	v_mfma_f32_16x16x32_bf16 v[100:103], v[64:67], v[188:191], v[100:103]
	v_mfma_f32_16x16x32_bf16 v[92:95], v[56:59], v[196:199], v[92:95]
	v_mfma_f32_16x16x32_bf16 v[84:87], v[64:67], v[196:199], v[84:87]
	v_mfma_f32_16x16x32_bf16 v[140:143], v[60:63], v[176:179], v[140:143]
	v_mfma_f32_16x16x32_bf16 v[132:135], v[72:75], v[176:179], v[132:135]
	v_mfma_f32_16x16x32_bf16 v[124:127], v[60:63], v[184:187], v[124:127]
	v_mfma_f32_16x16x32_bf16 v[116:119], v[72:75], v[184:187], v[116:119]
	v_mfma_f32_16x16x32_bf16 v[108:111], v[60:63], v[192:195], v[108:111]
	v_mfma_f32_16x16x32_bf16 v[100:103], v[72:75], v[192:195], v[100:103]
	v_mfma_f32_16x16x32_bf16 v[92:95], v[60:63], v[200:203], v[92:95]
	v_mfma_f32_16x16x32_bf16 v[84:87], v[72:75], v[200:203], v[84:87]
	v_mfma_f32_16x16x32_bf16 v[136:139], v[148:151], v[172:175], v[136:139]
	v_mfma_f32_16x16x32_bf16 v[128:131], v[164:167], v[172:175], v[128:131]
	v_mfma_f32_16x16x32_bf16 v[120:123], v[148:151], v[180:183], v[120:123]
	v_mfma_f32_16x16x32_bf16 v[112:115], v[164:167], v[180:183], v[112:115]
	v_mfma_f32_16x16x32_bf16 v[104:107], v[148:151], v[188:191], v[104:107]
	v_mfma_f32_16x16x32_bf16 v[96:99], v[164:167], v[188:191], v[96:99]
	v_mfma_f32_16x16x32_bf16 v[88:91], v[148:151], v[196:199], v[88:91]
	v_mfma_f32_16x16x32_bf16 v[80:83], v[164:167], v[196:199], v[80:83]
	v_mfma_f32_16x16x32_bf16 v[136:139], v[152:155], v[176:179], v[136:139]
	v_mfma_f32_16x16x32_bf16 v[128:131], v[168:171], v[176:179], v[128:131]
	v_mfma_f32_16x16x32_bf16 v[120:123], v[152:155], v[184:187], v[120:123]
	v_mfma_f32_16x16x32_bf16 v[112:115], v[168:171], v[184:187], v[112:115]
	v_mfma_f32_16x16x32_bf16 v[104:107], v[152:155], v[192:195], v[104:107]
	v_mfma_f32_16x16x32_bf16 v[96:99], v[168:171], v[192:195], v[96:99]
	v_mfma_f32_16x16x32_bf16 v[88:91], v[152:155], v[200:203], v[88:91]
	v_mfma_f32_16x16x32_bf16 v[80:83], v[168:171], v[200:203], v[80:83]
	s_setprio 0
	s_barrier
	s_add_u32 s78, s40, 0x80
	s_addc_u32 s79, s41, 0
	v_mov_b32_e32 v146, v158
	s_add_i32 s25, s25, s51
	ds_read_b128 v[172:175], v163 offset:49152
	ds_read_b128 v[176:179], v163 offset:50176
	ds_read_b128 v[180:183], v163 offset:51200
	ds_read_b128 v[184:187], v163 offset:52224
	ds_read_b128 v[188:191], v163 offset:53248
	ds_read_b128 v[192:195], v163 offset:54272
	ds_read_b128 v[196:199], v163 offset:55296
	ds_read_b128 v[200:203], v163 offset:56320
	s_mov_b32 m0, s25
	s_nop 0
	global_load_lds_dwordx4 v146, s[78:79]
	s_add_u32 s78, s40, 0x20080
	v_mov_b32_e32 v146, v158
	s_addc_u32 s79, s41, 0
	s_add_i32 m0, s25, 0x2000
	s_nop 0
	global_load_lds_dwordx4 v146, s[78:79]
	s_add_u32 s78, s40, 0x40080
	v_mov_b32_e32 v146, v158
	s_addc_u32 s79, s41, 0
	s_add_i32 s25, s37, s51
	s_mov_b32 m0, s25
	s_add_u32 s40, s40, 0x60080
	global_load_lds_dwordx4 v146, s[78:79]
	v_mov_b32_e32 v146, v158
	s_addc_u32 s41, s41, 0
	s_add_i32 m0, s25, 0x2000
	s_add_u32 s34, s34, 0x20080
	global_load_lds_dwordx4 v146, s[40:41]
	v_mov_b32_e32 v146, v159
	s_mov_b32 m0, s69
	s_addc_u32 s35, s35, 0
	global_load_lds_dwordx4 v146, s[38:39]
	v_mov_b32_e32 v146, v159
	s_mov_b32 m0, s70
	s_nop 0
	global_load_lds_dwordx4 v146, s[34:35]
	s_waitcnt vmcnt(8)
	s_waitcnt lgkmcnt(0)
	s_barrier
	s_setprio 3
	s_waitcnt lgkmcnt(0)
	v_mfma_f32_16x16x32_bf16 v[76:79], v[56:59], v[172:175], v[76:79]
	v_mfma_f32_16x16x32_bf16 v[68:71], v[64:67], v[172:175], v[68:71]
	v_mfma_f32_16x16x32_bf16 v[52:55], v[56:59], v[180:183], v[52:55]
	v_mfma_f32_16x16x32_bf16 v[36:39], v[64:67], v[180:183], v[36:39]
	v_mfma_f32_16x16x32_bf16 v[28:31], v[56:59], v[188:191], v[28:31]
	v_mfma_f32_16x16x32_bf16 v[20:23], v[64:67], v[188:191], v[20:23]
	v_mfma_f32_16x16x32_bf16 v[12:15], v[56:59], v[196:199], v[12:15]
	v_mfma_f32_16x16x32_bf16 v[4:7], v[64:67], v[196:199], v[4:7]
	v_mfma_f32_16x16x32_bf16 v[76:79], v[60:63], v[176:179], v[76:79]
	v_mfma_f32_16x16x32_bf16 v[68:71], v[72:75], v[176:179], v[68:71]
	v_mfma_f32_16x16x32_bf16 v[52:55], v[60:63], v[184:187], v[52:55]
	v_mfma_f32_16x16x32_bf16 v[36:39], v[72:75], v[184:187], v[36:39]
	v_mfma_f32_16x16x32_bf16 v[28:31], v[60:63], v[192:195], v[28:31]
	v_mfma_f32_16x16x32_bf16 v[20:23], v[72:75], v[192:195], v[20:23]
	v_mfma_f32_16x16x32_bf16 v[12:15], v[60:63], v[200:203], v[12:15]
	v_mfma_f32_16x16x32_bf16 v[4:7], v[72:75], v[200:203], v[4:7]
	v_mfma_f32_16x16x32_bf16 v[40:43], v[148:151], v[172:175], v[40:43]
	v_mfma_f32_16x16x32_bf16 v[72:75], v[152:155], v[176:179], v[40:43]
	v_mfma_f32_16x16x32_bf16 v[40:43], v[164:167], v[172:175], v[44:47]
	v_mfma_f32_16x16x32_bf16 v[64:67], v[168:171], v[176:179], v[40:43]
	v_mfma_f32_16x16x32_bf16 v[40:43], v[148:151], v[180:183], v[48:51]
	v_mfma_f32_16x16x32_bf16 v[32:35], v[164:167], v[180:183], v[32:35]
	v_mfma_f32_16x16x32_bf16 v[24:27], v[148:151], v[188:191], v[24:27]
	v_mfma_f32_16x16x32_bf16 v[16:19], v[164:167], v[188:191], v[16:19]
	v_mfma_f32_16x16x32_bf16 v[8:11], v[148:151], v[196:199], v[8:11]
	v_mfma_f32_16x16x32_bf16 v[0:3], v[164:167], v[196:199], v[0:3]
	v_mfma_f32_16x16x32_bf16 v[48:51], v[152:155], v[184:187], v[40:43]
	v_mfma_f32_16x16x32_bf16 v[32:35], v[168:171], v[184:187], v[32:35]
	v_mfma_f32_16x16x32_bf16 v[24:27], v[152:155], v[192:195], v[24:27]
	v_mfma_f32_16x16x32_bf16 v[16:19], v[168:171], v[192:195], v[16:19]
	v_mfma_f32_16x16x32_bf16 v[8:11], v[152:155], v[200:203], v[8:11]
	v_mfma_f32_16x16x32_bf16 v[0:3], v[168:171], v[200:203], v[0:3]
	s_setprio 0
	s_barrier
	s_add_i32 s23, s23, 2
	s_add_u32 s5, s5, 0x100
	s_addc_u32 s18, s18, 0
	s_add_u32 s30, s30, 0x100
	s_addc_u32 s31, s31, 0
	s_cmp_gt_u32 s23, 13
	s_cbranch_scc0 .LBB0_252
	s_and_b64 vcc, exec, s[20:21]
	s_cbranch_vccz .LBB0_255
	s_barrier

.LBB0_333:
	ds_read_b128 v[52:55], v38
	ds_read_b128 v[56:59], v38 offset:1024
	ds_read_b128 v[80:83], v38 offset:2048
	ds_read_b128 v[84:87], v38 offset:3072
	ds_read_b128 v[88:91], v39
	ds_read_b128 v[92:95], v39 offset:1024
	ds_read_b128 v[96:99], v39 offset:2048
	ds_read_b128 v[100:103], v39 offset:3072
	s_cmp_eq_u32 s34, 12
	s_cselect_b32 s14, s4, s30
	s_cselect_b32 s15, s5, s31
	s_cselect_b32 s18, s12, s28
	s_cselect_b32 s19, s13, s29
	s_add_u32 s16, s14, 0x80
	s_addc_u32 s17, s15, 0
	ds_read_b128 v[104:107], v40
	ds_read_b128 v[108:111], v40 offset:1024
	ds_read_b128 v[112:115], v40 offset:2048
	ds_read_b128 v[116:119], v40 offset:3072
	ds_read_b128 v[120:123], v40 offset:4096
	ds_read_b128 v[124:127], v40 offset:5120
	ds_read_b128 v[128:131], v40 offset:6144
	ds_read_b128 v[132:135], v40 offset:7168
	s_waitcnt vmcnt(6)
	s_waitcnt lgkmcnt(0)
	s_barrier
	s_setprio 3
	s_waitcnt lgkmcnt(0)
	v_mfma_f32_16x16x32_bf16 v[76:79], v[52:55], v[104:107], v[76:79]
	v_mfma_f32_16x16x32_bf16 v[68:71], v[80:83], v[104:107], v[68:71]
	v_mfma_f32_16x16x32_bf16 v[60:63], v[52:55], v[112:115], v[60:63]
	v_mfma_f32_16x16x32_bf16 v[44:47], v[80:83], v[112:115], v[44:47]
	v_mfma_f32_16x16x32_bf16 v[28:31], v[52:55], v[120:123], v[28:31]
	v_mfma_f32_16x16x32_bf16 v[20:23], v[80:83], v[120:123], v[20:23]
	v_mfma_f32_16x16x32_bf16 v[12:15], v[52:55], v[128:131], v[12:15]
	v_mfma_f32_16x16x32_bf16 v[4:7], v[80:83], v[128:131], v[4:7]
	v_mfma_f32_16x16x32_bf16 v[76:79], v[56:59], v[108:111], v[76:79]
	v_mfma_f32_16x16x32_bf16 v[68:71], v[84:87], v[108:111], v[68:71]
	v_mfma_f32_16x16x32_bf16 v[60:63], v[56:59], v[116:119], v[60:63]
	v_mfma_f32_16x16x32_bf16 v[44:47], v[84:87], v[116:119], v[44:47]
	v_mfma_f32_16x16x32_bf16 v[28:31], v[56:59], v[124:127], v[28:31]
	v_mfma_f32_16x16x32_bf16 v[20:23], v[84:87], v[124:127], v[20:23]
	v_mfma_f32_16x16x32_bf16 v[12:15], v[56:59], v[132:135], v[12:15]
	v_mfma_f32_16x16x32_bf16 v[4:7], v[84:87], v[132:135], v[4:7]
	v_mfma_f32_16x16x32_bf16 v[48:51], v[88:91], v[112:115], v[48:51]
	v_mfma_f32_16x16x32_bf16 v[32:35], v[96:99], v[112:115], v[32:35]
	v_mfma_f32_16x16x32_bf16 v[24:27], v[88:91], v[120:123], v[24:27]
	v_mfma_f32_16x16x32_bf16 v[16:19], v[96:99], v[120:123], v[16:19]
	v_mfma_f32_16x16x32_bf16 v[8:11], v[88:91], v[128:131], v[8:11]
	v_mfma_f32_16x16x32_bf16 v[0:3], v[96:99], v[128:131], v[0:3]
	v_mfma_f32_16x16x32_bf16 v[52:55], v[88:91], v[104:107], v[72:75]
	v_mfma_f32_16x16x32_bf16 v[56:59], v[96:99], v[104:107], v[64:67]
	v_mfma_f32_16x16x32_bf16 v[48:51], v[92:95], v[116:119], v[48:51]
	v_mfma_f32_16x16x32_bf16 v[32:35], v[100:103], v[116:119], v[32:35]
	v_mfma_f32_16x16x32_bf16 v[24:27], v[92:95], v[124:127], v[24:27]
	v_mfma_f32_16x16x32_bf16 v[16:19], v[100:103], v[124:127], v[16:19]
	v_mfma_f32_16x16x32_bf16 v[8:11], v[92:95], v[132:135], v[8:11]
	v_mfma_f32_16x16x32_bf16 v[0:3], v[100:103], v[132:135], v[0:3]
	v_mfma_f32_16x16x32_bf16 v[52:55], v[92:95], v[108:111], v[52:55]
	v_mfma_f32_16x16x32_bf16 v[56:59], v[100:103], v[108:111], v[56:59]
	s_setprio 0
	s_barrier
	v_mov_b32_e32 v43, v36
	s_mov_b64 s[50:51], s[18:19]
	s_mov_b32 m0, s35
	s_nop 0
	global_load_lds_dwordx4 v43, s[50:51]
	s_add_u32 s50, s18, 0x20000
	v_mov_b32_e32 v43, v36
	s_addc_u32 s51, s19, 0
	s_mov_b32 m0, s36
	s_nop 0
	global_load_lds_dwordx4 v43, s[50:51]
	s_add_u32 s50, s18, 0x40000
	v_mov_b32_e32 v43, v36
	s_addc_u32 s51, s19, 0
	s_mov_b32 m0, s37
	s_nop 0
	global_load_lds_dwordx4 v43, s[50:51]
	s_add_u32 s50, s18, 0x60000
	v_mov_b32_e32 v43, v36
	s_addc_u32 s51, s19, 0
	s_mov_b32 m0, s38
	s_nop 0
	global_load_lds_dwordx4 v43, s[50:51]
	v_mov_b32_e32 v43, v37
	s_mov_b64 s[50:51], s[14:15]
	s_mov_b32 m0, s23
	s_nop 0
	global_load_lds_dwordx4 v43, s[50:51]
	s_add_u32 s50, s14, 0x20000
	v_mov_b32_e32 v43, v37
	s_addc_u32 s51, s15, 0
	s_mov_b32 m0, s24
	s_nop 0
	global_load_lds_dwordx4 v43, s[50:51]
	s_waitcnt vmcnt(6)
	s_waitcnt lgkmcnt(0)
	s_barrier
	s_barrier
	ds_read_b128 v[64:67], v41
	ds_read_b128 v[72:75], v41 offset:1024
	ds_read_b128 v[80:83], v41 offset:2048
	ds_read_b128 v[84:87], v41 offset:3072
	ds_read_b128 v[88:91], v42
	ds_read_b128 v[92:95], v42 offset:1024
	ds_read_b128 v[96:99], v42 offset:2048
	ds_read_b128 v[100:103], v42 offset:3072
	ds_read_b128 v[104:107], v40 offset:32768
	ds_read_b128 v[108:111], v40 offset:33792
	ds_read_b128 v[112:115], v40 offset:34816
	ds_read_b128 v[116:119], v40 offset:35840
	ds_read_b128 v[120:123], v40 offset:36864
	ds_read_b128 v[124:127], v40 offset:37888
	ds_read_b128 v[128:131], v40 offset:38912
	ds_read_b128 v[132:135], v40 offset:39936
	s_waitcnt vmcnt(6)
	s_waitcnt lgkmcnt(0)
	s_barrier
	s_setprio 3
	s_waitcnt lgkmcnt(0)
	v_mfma_f32_16x16x32_bf16 v[76:79], v[64:67], v[104:107], v[76:79]
	v_mfma_f32_16x16x32_bf16 v[68:71], v[80:83], v[104:107], v[68:71]
	v_mfma_f32_16x16x32_bf16 v[60:63], v[64:67], v[112:115], v[60:63]
	v_mfma_f32_16x16x32_bf16 v[44:47], v[80:83], v[112:115], v[44:47]
	v_mfma_f32_16x16x32_bf16 v[28:31], v[64:67], v[120:123], v[28:31]
	v_mfma_f32_16x16x32_bf16 v[20:23], v[80:83], v[120:123], v[20:23]
	v_mfma_f32_16x16x32_bf16 v[12:15], v[64:67], v[128:131], v[12:15]
	v_mfma_f32_16x16x32_bf16 v[4:7], v[80:83], v[128:131], v[4:7]
	v_mfma_f32_16x16x32_bf16 v[76:79], v[72:75], v[108:111], v[76:79]
	v_mfma_f32_16x16x32_bf16 v[68:71], v[84:87], v[108:111], v[68:71]
	v_mfma_f32_16x16x32_bf16 v[60:63], v[72:75], v[116:119], v[60:63]
	v_mfma_f32_16x16x32_bf16 v[44:47], v[84:87], v[116:119], v[44:47]
	v_mfma_f32_16x16x32_bf16 v[28:31], v[72:75], v[124:127], v[28:31]
	v_mfma_f32_16x16x32_bf16 v[20:23], v[84:87], v[124:127], v[20:23]
	v_mfma_f32_16x16x32_bf16 v[12:15], v[72:75], v[132:135], v[12:15]
	v_mfma_f32_16x16x32_bf16 v[4:7], v[84:87], v[132:135], v[4:7]
	v_mfma_f32_16x16x32_bf16 v[52:55], v[88:91], v[104:107], v[52:55]
	s_add_u32 s50, s18, 0x80
	s_addc_u32 s51, s19, 0
	v_mfma_f32_16x16x32_bf16 v[72:75], v[92:95], v[108:111], v[52:55]
	v_mfma_f32_16x16x32_bf16 v[52:55], v[96:99], v[104:107], v[56:59]
	v_mfma_f32_16x16x32_bf16 v[48:51], v[88:91], v[112:115], v[48:51]
	v_mfma_f32_16x16x32_bf16 v[32:35], v[96:99], v[112:115], v[32:35]
	v_mfma_f32_16x16x32_bf16 v[24:27], v[88:91], v[120:123], v[24:27]
	v_mfma_f32_16x16x32_bf16 v[16:19], v[96:99], v[120:123], v[16:19]
	v_mfma_f32_16x16x32_bf16 v[8:11], v[88:91], v[128:131], v[8:11]
	v_mfma_f32_16x16x32_bf16 v[0:3], v[96:99], v[128:131], v[0:3]
	v_mfma_f32_16x16x32_bf16 v[64:67], v[100:103], v[108:111], v[52:55]
	v_mfma_f32_16x16x32_bf16 v[48:51], v[92:95], v[116:119], v[48:51]
	v_mfma_f32_16x16x32_bf16 v[32:35], v[100:103], v[116:119], v[32:35]
	v_mfma_f32_16x16x32_bf16 v[24:27], v[92:95], v[124:127], v[24:27]
	v_mfma_f32_16x16x32_bf16 v[16:19], v[100:103], v[124:127], v[16:19]
	v_mfma_f32_16x16x32_bf16 v[8:11], v[92:95], v[132:135], v[8:11]
	v_mfma_f32_16x16x32_bf16 v[0:3], v[100:103], v[132:135], v[0:3]
	s_setprio 0
	s_barrier
	v_mov_b32_e32 v43, v36
	s_mov_b32 m0, s39
	s_nop 0
	global_load_lds_dwordx4 v43, s[50:51]
	s_add_u32 s50, s18, 0x20080
	v_mov_b32_e32 v43, v36
	s_addc_u32 s51, s19, 0
	s_mov_b32 m0, s40
	s_nop 0
	global_load_lds_dwordx4 v43, s[50:51]
	v_mov_b32_e32 v43, v36
	s_add_u32 s50, s18, 0x40080
	s_addc_u32 s51, s19, 0
	s_mov_b32 m0, s41
	s_add_u32 s18, s18, 0x60080
	global_load_lds_dwordx4 v43, s[50:51]
	v_mov_b32_e32 v43, v36
	s_addc_u32 s19, s19, 0
	s_mov_b32 m0, s49
	s_add_u32 s14, s14, 0x20080
	global_load_lds_dwordx4 v43, s[18:19]
	v_mov_b32_e32 v43, v37
	s_mov_b32 m0, s26
	s_addc_u32 s15, s15, 0
	global_load_lds_dwordx4 v43, s[16:17]
	v_mov_b32_e32 v43, v37
	s_mov_b32 m0, s27
	s_nop 0
	global_load_lds_dwordx4 v43, s[14:15]
	s_waitcnt vmcnt(6)
	s_waitcnt lgkmcnt(0)
	s_barrier
	s_barrier
	s_add_i32 s34, s34, 2
	s_add_u32 s28, s28, 0x100
	s_addc_u32 s29, s29, 0
	s_add_u32 s30, s30, 0x100
	s_addc_u32 s31, s31, 0
	s_cmp_gt_u32 s34, 13
	s_cbranch_scc0 .LBB0_333
	s_cmpk_lt_u32 s1, 0x100
	s_cbranch_scc0 .LBB0_336
	s_barrier

.LBB0_725:
	ds_read_b128 v[130:133], v177
	ds_read_b128 v[134:137], v177 offset:1024
	ds_read_b128 v[138:141], v177 offset:2048
	ds_read_b128 v[142:145], v177 offset:3072
	ds_read_b128 v[146:149], v178
	ds_read_b128 v[150:153], v178 offset:1024
	ds_read_b128 v[154:157], v178 offset:2048
	ds_read_b128 v[158:161], v178 offset:3072
	s_add_u32 s26, s24, 0xfffa0080
	s_addc_u32 s27, s25, -1
	s_cmp_eq_u32 s60, 12
	s_cselect_b32 s26, s18, s26
	s_cselect_b32 s27, s19, s27
	s_cselect_b32 s30, s20, s15
	s_cselect_b32 s31, s21, s17
	s_add_u32 s28, s26, 0x80
	s_addc_u32 s29, s27, 0
	s_add_u32 s64, s24, 0xfffe0000
	v_mov_b32_e32 v200, v175
	s_addc_u32 s65, s25, -1
	ds_read_b128 v[162:165], v179
	ds_read_b128 v[166:169], v179 offset:1024
	ds_read_b128 v[170:173], v179 offset:2048
	ds_read_b128 v[180:183], v179 offset:3072
	ds_read_b128 v[184:187], v179 offset:4096
	ds_read_b128 v[188:191], v179 offset:5120
	ds_read_b128 v[192:195], v179 offset:6144
	ds_read_b128 v[196:199], v179 offset:7168
	s_add_i32 m0, s23, 0xc000
	s_nop 0
	global_load_lds_dwordx4 v200, s[64:65]
	v_mov_b32_e32 v200, v175
	s_mov_b64 s[64:65], s[24:25]
	s_add_i32 m0, s23, 0xe000
	s_nop 0
	global_load_lds_dwordx4 v200, s[64:65]
	s_waitcnt vmcnt(8)
	s_waitcnt lgkmcnt(0)
	s_barrier
	s_setprio 3
	s_waitcnt lgkmcnt(0)
	v_mfma_f32_16x16x32_bf16 v[124:127], v[130:133], v[162:165], v[124:127]
	v_mfma_f32_16x16x32_bf16 v[120:123], v[138:141], v[162:165], v[120:123]
	v_mfma_f32_16x16x32_bf16 v[108:111], v[130:133], v[170:173], v[108:111]
	v_mfma_f32_16x16x32_bf16 v[104:107], v[138:141], v[170:173], v[104:107]
	v_mfma_f32_16x16x32_bf16 v[92:95], v[130:133], v[184:187], v[92:95]
	v_mfma_f32_16x16x32_bf16 v[88:91], v[138:141], v[184:187], v[88:91]
	v_mfma_f32_16x16x32_bf16 v[76:79], v[130:133], v[192:195], v[76:79]
	v_mfma_f32_16x16x32_bf16 v[72:75], v[138:141], v[192:195], v[72:75]
	v_mfma_f32_16x16x32_bf16 v[124:127], v[134:137], v[166:169], v[124:127]
	v_mfma_f32_16x16x32_bf16 v[120:123], v[142:145], v[166:169], v[120:123]
	v_mfma_f32_16x16x32_bf16 v[108:111], v[134:137], v[180:183], v[108:111]
	v_mfma_f32_16x16x32_bf16 v[104:107], v[142:145], v[180:183], v[104:107]
	v_mfma_f32_16x16x32_bf16 v[92:95], v[134:137], v[188:191], v[92:95]
	v_mfma_f32_16x16x32_bf16 v[88:91], v[142:145], v[188:191], v[88:91]
	v_mfma_f32_16x16x32_bf16 v[76:79], v[134:137], v[196:199], v[76:79]
	v_mfma_f32_16x16x32_bf16 v[72:75], v[142:145], v[196:199], v[72:75]
	v_mfma_f32_16x16x32_bf16 v[116:119], v[146:149], v[162:165], v[116:119]
	v_mfma_f32_16x16x32_bf16 v[112:115], v[154:157], v[162:165], v[112:115]
	v_mfma_f32_16x16x32_bf16 v[100:103], v[146:149], v[170:173], v[100:103]
	v_mfma_f32_16x16x32_bf16 v[96:99], v[154:157], v[170:173], v[96:99]
	v_mfma_f32_16x16x32_bf16 v[84:87], v[146:149], v[184:187], v[84:87]
	v_mfma_f32_16x16x32_bf16 v[80:83], v[154:157], v[184:187], v[80:83]
	v_mfma_f32_16x16x32_bf16 v[68:71], v[146:149], v[192:195], v[68:71]
	v_mfma_f32_16x16x32_bf16 v[64:67], v[154:157], v[192:195], v[64:67]
	v_mfma_f32_16x16x32_bf16 v[116:119], v[150:153], v[166:169], v[116:119]
	v_mfma_f32_16x16x32_bf16 v[112:115], v[158:161], v[166:169], v[112:115]
	v_mfma_f32_16x16x32_bf16 v[100:103], v[150:153], v[180:183], v[100:103]
	v_mfma_f32_16x16x32_bf16 v[96:99], v[158:161], v[180:183], v[96:99]
	v_mfma_f32_16x16x32_bf16 v[84:87], v[150:153], v[188:191], v[84:87]
	v_mfma_f32_16x16x32_bf16 v[80:83], v[158:161], v[188:191], v[80:83]
	v_mfma_f32_16x16x32_bf16 v[68:71], v[150:153], v[196:199], v[68:71]
	v_mfma_f32_16x16x32_bf16 v[64:67], v[158:161], v[196:199], v[64:67]
	s_setprio 0
	s_barrier
	v_mov_b32_e32 v200, v174
	s_mov_b64 s[64:65], s[30:31]
	s_add_i32 s61, s51, s36
	ds_read_b128 v[162:165], v179 offset:16384
	ds_read_b128 v[166:169], v179 offset:17408
	ds_read_b128 v[170:173], v179 offset:18432
	ds_read_b128 v[180:183], v179 offset:19456
	ds_read_b128 v[184:187], v179 offset:20480
	ds_read_b128 v[188:191], v179 offset:21504
	ds_read_b128 v[192:195], v179 offset:22528
	ds_read_b128 v[196:199], v179 offset:23552
	s_mov_b32 m0, s61
	s_nop 0
	global_load_lds_dwordx4 v200, s[64:65]
	s_add_u32 s64, s30, 0x20000
	v_mov_b32_e32 v200, v174
	s_addc_u32 s65, s31, 0
	s_add_i32 m0, s61, 0x2000
	s_nop 0
	global_load_lds_dwordx4 v200, s[64:65]
	s_add_u32 s64, s30, 0x40000
	v_mov_b32_e32 v200, v174
	s_addc_u32 s65, s31, 0
	s_add_i32 s61, s52, s36
	s_mov_b32 m0, s61
	s_nop 0
	global_load_lds_dwordx4 v200, s[64:65]
	s_add_u32 s64, s30, 0x60000
	v_mov_b32_e32 v200, v174
	s_addc_u32 s65, s31, 0
	s_add_i32 m0, s61, 0x2000
	s_nop 0
	global_load_lds_dwordx4 v200, s[64:65]
	v_mov_b32_e32 v200, v175
	s_mov_b64 s[64:65], s[26:27]
	s_mov_b32 m0, s23
	s_nop 0
	global_load_lds_dwordx4 v200, s[64:65]
	s_add_u32 s64, s26, 0x20000
	v_mov_b32_e32 v200, v175
	s_addc_u32 s65, s27, 0
	s_mov_b32 m0, s38
	s_nop 0
	global_load_lds_dwordx4 v200, s[64:65]
	s_waitcnt vmcnt(8)
	s_waitcnt lgkmcnt(0)
	s_barrier
	s_setprio 3
	s_waitcnt lgkmcnt(0)
	v_mfma_f32_16x16x32_bf16 v[60:63], v[130:133], v[162:165], v[60:63]
	v_mfma_f32_16x16x32_bf16 v[56:59], v[138:141], v[162:165], v[56:59]
	v_mfma_f32_16x16x32_bf16 v[44:47], v[130:133], v[170:173], v[44:47]
	v_mfma_f32_16x16x32_bf16 v[40:43], v[138:141], v[170:173], v[40:43]
	v_mfma_f32_16x16x32_bf16 v[28:31], v[130:133], v[184:187], v[28:31]
	v_mfma_f32_16x16x32_bf16 v[24:27], v[138:141], v[184:187], v[24:27]
	v_mfma_f32_16x16x32_bf16 v[12:15], v[130:133], v[192:195], v[12:15]
	v_mfma_f32_16x16x32_bf16 v[8:11], v[138:141], v[192:195], v[8:11]
	v_mfma_f32_16x16x32_bf16 v[60:63], v[134:137], v[166:169], v[60:63]
	v_mfma_f32_16x16x32_bf16 v[56:59], v[142:145], v[166:169], v[56:59]
	v_mfma_f32_16x16x32_bf16 v[44:47], v[134:137], v[180:183], v[44:47]
	v_mfma_f32_16x16x32_bf16 v[40:43], v[142:145], v[180:183], v[40:43]
	v_mfma_f32_16x16x32_bf16 v[28:31], v[134:137], v[188:191], v[28:31]
	v_mfma_f32_16x16x32_bf16 v[24:27], v[142:145], v[188:191], v[24:27]
	v_mfma_f32_16x16x32_bf16 v[12:15], v[134:137], v[196:199], v[12:15]
	v_mfma_f32_16x16x32_bf16 v[8:11], v[142:145], v[196:199], v[8:11]
	v_mfma_f32_16x16x32_bf16 v[52:55], v[146:149], v[162:165], v[52:55]
	v_mfma_f32_16x16x32_bf16 v[48:51], v[154:157], v[162:165], v[48:51]
	v_mfma_f32_16x16x32_bf16 v[36:39], v[146:149], v[170:173], v[36:39]
	v_mfma_f32_16x16x32_bf16 v[32:35], v[154:157], v[170:173], v[32:35]
	v_mfma_f32_16x16x32_bf16 v[20:23], v[146:149], v[184:187], v[20:23]
	v_mfma_f32_16x16x32_bf16 v[16:19], v[154:157], v[184:187], v[16:19]
	v_mfma_f32_16x16x32_bf16 v[4:7], v[146:149], v[192:195], v[4:7]
	v_mfma_f32_16x16x32_bf16 v[0:3], v[154:157], v[192:195], v[0:3]
	v_mfma_f32_16x16x32_bf16 v[52:55], v[150:153], v[166:169], v[52:55]
	v_mfma_f32_16x16x32_bf16 v[48:51], v[158:161], v[166:169], v[48:51]
	v_mfma_f32_16x16x32_bf16 v[36:39], v[150:153], v[180:183], v[36:39]
	v_mfma_f32_16x16x32_bf16 v[32:35], v[158:161], v[180:183], v[32:35]
	v_mfma_f32_16x16x32_bf16 v[20:23], v[150:153], v[188:191], v[20:23]
	v_mfma_f32_16x16x32_bf16 v[16:19], v[158:161], v[188:191], v[16:19]
	v_mfma_f32_16x16x32_bf16 v[4:7], v[150:153], v[196:199], v[4:7]
	v_mfma_f32_16x16x32_bf16 v[0:3], v[158:161], v[196:199], v[0:3]
	s_setprio 0
	s_barrier
	s_add_i32 s61, 0, 0x18000
	s_add_i32 s68, 0, 0x1c000
	v_add_u32_e32 v142, s61, v176
	v_add_u32_e32 v158, s68, v176
	ds_read_b128 v[130:133], v142
	ds_read_b128 v[134:137], v142 offset:1024
	ds_read_b128 v[138:141], v142 offset:2048
	ds_read_b128 v[142:145], v142 offset:3072
	ds_read_b128 v[146:149], v158
	ds_read_b128 v[150:153], v158 offset:1024
	ds_read_b128 v[154:157], v158 offset:2048
	ds_read_b128 v[158:161], v158 offset:3072
	s_add_u32 s64, s26, 0x40000
	v_mov_b32_e32 v200, v175
	s_addc_u32 s65, s27, 0
	s_mov_b32 m0, s39
	ds_read_b128 v[162:165], v179 offset:32768
	ds_read_b128 v[166:169], v179 offset:33792
	ds_read_b128 v[170:173], v179 offset:34816
	ds_read_b128 v[180:183], v179 offset:35840
	ds_read_b128 v[184:187], v179 offset:36864
	ds_read_b128 v[188:191], v179 offset:37888
	ds_read_b128 v[192:195], v179 offset:38912
	ds_read_b128 v[196:199], v179 offset:39936
	s_nop 0
	global_load_lds_dwordx4 v200, s[64:65]
	s_add_u32 s64, s26, 0x60000
	v_mov_b32_e32 v200, v175
	s_addc_u32 s65, s27, 0
	s_mov_b32 m0, s40
	s_nop 0
	global_load_lds_dwordx4 v200, s[64:65]
	s_waitcnt vmcnt(8)
	s_waitcnt lgkmcnt(0)
	s_barrier
	s_setprio 3
	s_waitcnt lgkmcnt(0)
	v_mfma_f32_16x16x32_bf16 v[124:127], v[130:133], v[162:165], v[124:127]
	v_mfma_f32_16x16x32_bf16 v[120:123], v[138:141], v[162:165], v[120:123]
	v_mfma_f32_16x16x32_bf16 v[108:111], v[130:133], v[170:173], v[108:111]
	v_mfma_f32_16x16x32_bf16 v[104:107], v[138:141], v[170:173], v[104:107]
	v_mfma_f32_16x16x32_bf16 v[92:95], v[130:133], v[184:187], v[92:95]
	v_mfma_f32_16x16x32_bf16 v[88:91], v[138:141], v[184:187], v[88:91]
	v_mfma_f32_16x16x32_bf16 v[76:79], v[130:133], v[192:195], v[76:79]
	v_mfma_f32_16x16x32_bf16 v[72:75], v[138:141], v[192:195], v[72:75]
	v_mfma_f32_16x16x32_bf16 v[124:127], v[134:137], v[166:169], v[124:127]
	v_mfma_f32_16x16x32_bf16 v[120:123], v[142:145], v[166:169], v[120:123]
	v_mfma_f32_16x16x32_bf16 v[108:111], v[134:137], v[180:183], v[108:111]
	v_mfma_f32_16x16x32_bf16 v[104:107], v[142:145], v[180:183], v[104:107]
	v_mfma_f32_16x16x32_bf16 v[92:95], v[134:137], v[188:191], v[92:95]
	v_mfma_f32_16x16x32_bf16 v[88:91], v[142:145], v[188:191], v[88:91]
	v_mfma_f32_16x16x32_bf16 v[76:79], v[134:137], v[196:199], v[76:79]
	v_mfma_f32_16x16x32_bf16 v[72:75], v[142:145], v[196:199], v[72:75]
	v_mfma_f32_16x16x32_bf16 v[116:119], v[146:149], v[162:165], v[116:119]
	v_mfma_f32_16x16x32_bf16 v[112:115], v[154:157], v[162:165], v[112:115]
	v_mfma_f32_16x16x32_bf16 v[100:103], v[146:149], v[170:173], v[100:103]
	v_mfma_f32_16x16x32_bf16 v[96:99], v[154:157], v[170:173], v[96:99]
	v_mfma_f32_16x16x32_bf16 v[84:87], v[146:149], v[184:187], v[84:87]
	v_mfma_f32_16x16x32_bf16 v[80:83], v[154:157], v[184:187], v[80:83]
	v_mfma_f32_16x16x32_bf16 v[68:71], v[146:149], v[192:195], v[68:71]
	v_mfma_f32_16x16x32_bf16 v[64:67], v[154:157], v[192:195], v[64:67]
	v_mfma_f32_16x16x32_bf16 v[116:119], v[150:153], v[166:169], v[116:119]
	v_mfma_f32_16x16x32_bf16 v[112:115], v[158:161], v[166:169], v[112:115]
	v_mfma_f32_16x16x32_bf16 v[100:103], v[150:153], v[180:183], v[100:103]
	v_mfma_f32_16x16x32_bf16 v[96:99], v[158:161], v[180:183], v[96:99]
	v_mfma_f32_16x16x32_bf16 v[84:87], v[150:153], v[188:191], v[84:87]
	v_mfma_f32_16x16x32_bf16 v[80:83], v[158:161], v[188:191], v[80:83]
	v_mfma_f32_16x16x32_bf16 v[68:71], v[150:153], v[196:199], v[68:71]
	v_mfma_f32_16x16x32_bf16 v[64:67], v[158:161], v[196:199], v[64:67]
	s_setprio 0
	s_barrier
	s_add_u32 s64, s30, 0x80
	s_addc_u32 s65, s31, 0
	v_mov_b32_e32 v200, v174
	s_add_i32 s61, s61, s36
	ds_read_b128 v[162:165], v179 offset:49152
	ds_read_b128 v[166:169], v179 offset:50176
	ds_read_b128 v[170:173], v179 offset:51200
	ds_read_b128 v[180:183], v179 offset:52224
	ds_read_b128 v[184:187], v179 offset:53248
	ds_read_b128 v[188:191], v179 offset:54272
	ds_read_b128 v[192:195], v179 offset:55296
	ds_read_b128 v[196:199], v179 offset:56320
	s_mov_b32 m0, s61
	s_nop 0
	global_load_lds_dwordx4 v200, s[64:65]
	s_add_u32 s64, s30, 0x20080
	v_mov_b32_e32 v200, v174
	s_addc_u32 s65, s31, 0
	s_add_i32 m0, s61, 0x2000
	s_nop 0
	global_load_lds_dwordx4 v200, s[64:65]
	s_add_u32 s64, s30, 0x40080
	v_mov_b32_e32 v200, v174
	s_addc_u32 s65, s31, 0
	s_add_i32 s61, s68, s36
	s_mov_b32 m0, s61
	s_add_u32 s30, s30, 0x60080
	global_load_lds_dwordx4 v200, s[64:65]
	v_mov_b32_e32 v200, v174
	s_addc_u32 s31, s31, 0
	s_add_i32 m0, s61, 0x2000
	s_add_u32 s26, s26, 0x20080
	global_load_lds_dwordx4 v200, s[30:31]
	v_mov_b32_e32 v200, v175
	s_mov_b32 m0, s48
	s_addc_u32 s27, s27, 0
	global_load_lds_dwordx4 v200, s[28:29]
	v_mov_b32_e32 v200, v175
	s_mov_b32 m0, s49
	s_nop 0
	global_load_lds_dwordx4 v200, s[26:27]
	s_waitcnt vmcnt(8)
	s_waitcnt lgkmcnt(0)
	s_barrier
	s_setprio 3
	s_waitcnt lgkmcnt(0)
	v_mfma_f32_16x16x32_bf16 v[60:63], v[130:133], v[162:165], v[60:63]
	v_mfma_f32_16x16x32_bf16 v[56:59], v[138:141], v[162:165], v[56:59]
	v_mfma_f32_16x16x32_bf16 v[44:47], v[130:133], v[170:173], v[44:47]
	v_mfma_f32_16x16x32_bf16 v[40:43], v[138:141], v[170:173], v[40:43]
	v_mfma_f32_16x16x32_bf16 v[28:31], v[130:133], v[184:187], v[28:31]
	v_mfma_f32_16x16x32_bf16 v[24:27], v[138:141], v[184:187], v[24:27]
	v_mfma_f32_16x16x32_bf16 v[12:15], v[130:133], v[192:195], v[12:15]
	v_mfma_f32_16x16x32_bf16 v[8:11], v[138:141], v[192:195], v[8:11]
	v_mfma_f32_16x16x32_bf16 v[60:63], v[134:137], v[166:169], v[60:63]
	v_mfma_f32_16x16x32_bf16 v[56:59], v[142:145], v[166:169], v[56:59]
	v_mfma_f32_16x16x32_bf16 v[44:47], v[134:137], v[180:183], v[44:47]
	v_mfma_f32_16x16x32_bf16 v[40:43], v[142:145], v[180:183], v[40:43]
	v_mfma_f32_16x16x32_bf16 v[28:31], v[134:137], v[188:191], v[28:31]
	v_mfma_f32_16x16x32_bf16 v[24:27], v[142:145], v[188:191], v[24:27]
	v_mfma_f32_16x16x32_bf16 v[12:15], v[134:137], v[196:199], v[12:15]
	v_mfma_f32_16x16x32_bf16 v[8:11], v[142:145], v[196:199], v[8:11]
	v_mfma_f32_16x16x32_bf16 v[52:55], v[146:149], v[162:165], v[52:55]
	v_mfma_f32_16x16x32_bf16 v[48:51], v[154:157], v[162:165], v[48:51]
	v_mfma_f32_16x16x32_bf16 v[36:39], v[146:149], v[170:173], v[36:39]
	v_mfma_f32_16x16x32_bf16 v[32:35], v[154:157], v[170:173], v[32:35]
	v_mfma_f32_16x16x32_bf16 v[20:23], v[146:149], v[184:187], v[20:23]
	v_mfma_f32_16x16x32_bf16 v[16:19], v[154:157], v[184:187], v[16:19]
	v_mfma_f32_16x16x32_bf16 v[4:7], v[146:149], v[192:195], v[4:7]
	v_mfma_f32_16x16x32_bf16 v[0:3], v[154:157], v[192:195], v[0:3]
	v_mfma_f32_16x16x32_bf16 v[52:55], v[150:153], v[166:169], v[52:55]
	v_mfma_f32_16x16x32_bf16 v[48:51], v[158:161], v[166:169], v[48:51]
	v_mfma_f32_16x16x32_bf16 v[36:39], v[150:153], v[180:183], v[36:39]
	v_mfma_f32_16x16x32_bf16 v[32:35], v[158:161], v[180:183], v[32:35]
	v_mfma_f32_16x16x32_bf16 v[20:23], v[150:153], v[188:191], v[20:23]
	v_mfma_f32_16x16x32_bf16 v[16:19], v[158:161], v[188:191], v[16:19]
	v_mfma_f32_16x16x32_bf16 v[4:7], v[150:153], v[196:199], v[4:7]
	v_mfma_f32_16x16x32_bf16 v[0:3], v[158:161], v[196:199], v[0:3]
	s_setprio 0
	s_barrier
	s_add_i32 s60, s60, 2
	s_add_u32 s15, s15, 0x100
	s_addc_u32 s17, s17, 0
	s_add_u32 s24, s24, 0x100
	s_addc_u32 s25, s25, 0
	s_cmp_gt_u32 s60, 13
	s_cbranch_scc0 .LBB0_725
	s_and_b64 vcc, exec, s[10:11]
	s_cbranch_vccz .LBB0_728
	s_barrier

.LBB0_1124:
	ds_read_b128 v[144:147], v137
	ds_read_b128 v[148:151], v137 offset:1024
	ds_read_b128 v[152:155], v137 offset:2048
	ds_read_b128 v[156:159], v137 offset:3072
	ds_read_b128 v[160:163], v138
	ds_read_b128 v[164:167], v138 offset:1024
	ds_read_b128 v[168:171], v138 offset:2048
	ds_read_b128 v[172:175], v138 offset:3072
	s_cmp_eq_u32 s70, 4
	s_cselect_b64 vcc, -1, 0
	s_and_b64 s[22:23], vcc, exec
	s_cselect_b32 s26, s8, s68
	s_cselect_b32 s27, s9, s69
	s_cselect_b32 s24, s20, s14
	s_cselect_b32 s25, s21, s65
	s_add_u32 s22, s26, 0x80
	s_addc_u32 s23, s27, 0
	s_add_u32 s72, s68, 0xffffff80
	s_addc_u32 s73, s69, -1
	v_mov_b32_e32 v132, v130
	s_mov_b32 m0, s49
	ds_read_b128 v[176:179], v139
	ds_read_b128 v[180:183], v139 offset:1024
	ds_read_b128 v[184:187], v139 offset:2048
	ds_read_b128 v[188:191], v139 offset:3072
	ds_read_b128 v[192:195], v139 offset:4096
	ds_read_b128 v[196:199], v139 offset:5120
	ds_read_b128 v[200:203], v139 offset:6144
	ds_read_b128 v[204:207], v139 offset:7168
	s_mov_b64 s[74:75], s[72:73]
	s_nop 0
	global_load_lds_dwordx4 v132, s[74:75]
	v_mov_b32_e32 v132, v131
	s_mov_b32 m0, s51
	s_nop 0
	global_load_lds_dwordx4 v132, s[72:73]
	s_waitcnt vmcnt(8)
	s_waitcnt lgkmcnt(0)
	s_barrier
	s_setprio 3
	s_waitcnt lgkmcnt(0)
	v_mfma_f32_16x16x128_f8f6f4 v[124:127], v[144:151], v[176:183], v[124:127]
	v_mfma_f32_16x16x128_f8f6f4 v[116:119], v[152:159], v[176:183], v[116:119]
	v_mfma_f32_16x16x128_f8f6f4 v[108:111], v[144:151], v[184:191], v[108:111]
	v_mfma_f32_16x16x128_f8f6f4 v[100:103], v[152:159], v[184:191], v[100:103]
	v_mfma_f32_16x16x128_f8f6f4 v[92:95], v[144:151], v[192:199], v[92:95]
	v_mfma_f32_16x16x128_f8f6f4 v[84:87], v[152:159], v[192:199], v[84:87]
	v_mfma_f32_16x16x128_f8f6f4 v[76:79], v[144:151], v[200:207], v[76:79]
	v_mfma_f32_16x16x128_f8f6f4 v[68:71], v[152:159], v[200:207], v[68:71]
	v_mfma_f32_16x16x128_f8f6f4 v[120:123], v[160:167], v[176:183], v[120:123]
	v_mfma_f32_16x16x128_f8f6f4 v[112:115], v[168:175], v[176:183], v[112:115]
	v_mfma_f32_16x16x128_f8f6f4 v[104:107], v[160:167], v[184:191], v[104:107]
	v_mfma_f32_16x16x128_f8f6f4 v[96:99], v[168:175], v[184:191], v[96:99]
	v_mfma_f32_16x16x128_f8f6f4 v[88:91], v[160:167], v[192:199], v[88:91]
	v_mfma_f32_16x16x128_f8f6f4 v[80:83], v[168:175], v[192:199], v[80:83]
	v_mfma_f32_16x16x128_f8f6f4 v[72:75], v[160:167], v[200:207], v[72:75]
	v_mfma_f32_16x16x128_f8f6f4 v[64:67], v[168:175], v[200:207], v[64:67]
	s_setprio 0
	s_barrier
	v_mov_b32_e32 v132, v134
	s_mov_b64 s[72:73], s[24:25]
	s_mov_b32 m0, s52
	ds_read_b128 v[176:179], v139 offset:16384
	ds_read_b128 v[180:183], v139 offset:17408
	ds_read_b128 v[184:187], v139 offset:18432
	ds_read_b128 v[188:191], v139 offset:19456
	ds_read_b128 v[192:195], v139 offset:20480
	ds_read_b128 v[196:199], v139 offset:21504
	ds_read_b128 v[200:203], v139 offset:22528
	ds_read_b128 v[204:207], v139 offset:23552
	s_nop 0
	global_load_lds_dwordx4 v132, s[72:73]
	s_add_u32 s72, s24, 0x10000
	v_mov_b32_e32 v132, v134
	s_addc_u32 s73, s25, 0
	s_add_i32 m0, s52, 0x2000
	s_nop 0
	global_load_lds_dwordx4 v132, s[72:73]
	s_add_u32 s72, s24, 0x20000
	v_mov_b32_e32 v132, v134
	s_addc_u32 s73, s25, 0
	s_add_i32 s71, s48, s35
	s_mov_b32 m0, s71
	s_nop 0
	global_load_lds_dwordx4 v132, s[72:73]
	v_mov_b32_e32 v132, v134
	s_add_u32 s72, s24, 0x30000
	s_addc_u32 s73, s25, 0
	s_add_i32 m0, s71, 0x2000
	s_nop 0
	global_load_lds_dwordx4 v132, s[72:73]
	v_cndmask_b32_e32 v132, v128, v141, vcc
	v_lshlrev_b32_e32 v133, 10, v132
	v_and_or_b32 v133, v133, s37, v135
	v_mov_b32_e32 v143, v133
	s_mov_b64 s[72:73], s[26:27]
	s_mov_b32 m0, s36
	s_nop 0
	global_load_lds_dwordx4 v143, s[72:73]
	v_cndmask_b32_e32 v143, v129, v142, vcc
	v_lshlrev_b32_e32 v208, 10, v143
	v_and_or_b32 v208, v208, s37, v135
	v_mov_b32_e32 v209, v208
	s_mov_b64 s[72:73], s[26:27]
	s_mov_b32 m0, s38
	s_nop 0
	global_load_lds_dwordx4 v209, s[72:73]
	s_waitcnt vmcnt(8)
	s_waitcnt lgkmcnt(0)
	s_barrier
	s_setprio 3
	s_waitcnt lgkmcnt(0)
	v_mfma_f32_16x16x128_f8f6f4 v[60:63], v[144:151], v[176:183], v[60:63]
	v_mfma_f32_16x16x128_f8f6f4 v[52:55], v[152:159], v[176:183], v[52:55]
	v_mfma_f32_16x16x128_f8f6f4 v[44:47], v[144:151], v[184:191], v[44:47]
	v_mfma_f32_16x16x128_f8f6f4 v[36:39], v[152:159], v[184:191], v[36:39]
	v_mfma_f32_16x16x128_f8f6f4 v[28:31], v[144:151], v[192:199], v[28:31]
	v_mfma_f32_16x16x128_f8f6f4 v[20:23], v[152:159], v[192:199], v[20:23]
	v_mfma_f32_16x16x128_f8f6f4 v[12:15], v[144:151], v[200:207], v[12:15]
	v_mfma_f32_16x16x128_f8f6f4 v[4:7], v[152:159], v[200:207], v[4:7]
	v_mfma_f32_16x16x128_f8f6f4 v[56:59], v[160:167], v[176:183], v[56:59]
	v_mfma_f32_16x16x128_f8f6f4 v[48:51], v[168:175], v[176:183], v[48:51]
	v_mfma_f32_16x16x128_f8f6f4 v[40:43], v[160:167], v[184:191], v[40:43]
	v_mfma_f32_16x16x128_f8f6f4 v[32:35], v[168:175], v[184:191], v[32:35]
	v_mfma_f32_16x16x128_f8f6f4 v[24:27], v[160:167], v[192:199], v[24:27]
	v_mfma_f32_16x16x128_f8f6f4 v[16:19], v[168:175], v[192:199], v[16:19]
	v_mfma_f32_16x16x128_f8f6f4 v[8:11], v[160:167], v[200:207], v[8:11]
	v_mfma_f32_16x16x128_f8f6f4 v[0:3], v[168:175], v[200:207], v[0:3]
	s_setprio 0
	s_barrier
	s_add_i32 s71, 0, 0x18000
	s_add_i32 s74, 0, 0x1c000
	v_add_u32_e32 v156, s71, v136
	v_add_u32_e32 v172, s74, v136
	ds_read_b128 v[144:147], v156
	ds_read_b128 v[148:151], v156 offset:1024
	ds_read_b128 v[152:155], v156 offset:2048
	ds_read_b128 v[156:159], v156 offset:3072
	ds_read_b128 v[160:163], v172
	ds_read_b128 v[164:167], v172 offset:1024
	ds_read_b128 v[168:171], v172 offset:2048
	ds_read_b128 v[172:175], v172 offset:3072
	v_bfe_u32 v132, v132, 16, 16
	v_lshl_or_b32 v132, v132, 10, v135
	s_mov_b32 m0, s39
	ds_read_b128 v[176:179], v139 offset:32768
	ds_read_b128 v[180:183], v139 offset:33792
	ds_read_b128 v[184:187], v139 offset:34816
	ds_read_b128 v[188:191], v139 offset:35840
	ds_read_b128 v[192:195], v139 offset:36864
	ds_read_b128 v[196:199], v139 offset:37888
	ds_read_b128 v[200:203], v139 offset:38912
	ds_read_b128 v[204:207], v139 offset:39936
	s_mov_b64 s[72:73], s[26:27]
	s_nop 0
	global_load_lds_dwordx4 v132, s[72:73]
	v_bfe_u32 v132, v143, 16, 16
	v_lshl_or_b32 v132, v132, 10, v135
	s_mov_b32 m0, s40
	s_nop 0
	global_load_lds_dwordx4 v132, s[26:27]
	s_waitcnt vmcnt(8)
	s_waitcnt lgkmcnt(0)
	s_barrier
	s_setprio 3
	s_waitcnt lgkmcnt(0)
	v_mfma_f32_16x16x128_f8f6f4 v[124:127], v[144:151], v[176:183], v[124:127]
	v_mfma_f32_16x16x128_f8f6f4 v[116:119], v[152:159], v[176:183], v[116:119]
	v_mfma_f32_16x16x128_f8f6f4 v[108:111], v[144:151], v[184:191], v[108:111]
	v_mfma_f32_16x16x128_f8f6f4 v[100:103], v[152:159], v[184:191], v[100:103]
	v_mfma_f32_16x16x128_f8f6f4 v[92:95], v[144:151], v[192:199], v[92:95]
	v_mfma_f32_16x16x128_f8f6f4 v[84:87], v[152:159], v[192:199], v[84:87]
	v_mfma_f32_16x16x128_f8f6f4 v[76:79], v[144:151], v[200:207], v[76:79]
	v_mfma_f32_16x16x128_f8f6f4 v[68:71], v[152:159], v[200:207], v[68:71]
	v_mfma_f32_16x16x128_f8f6f4 v[120:123], v[160:167], v[176:183], v[120:123]
	v_mfma_f32_16x16x128_f8f6f4 v[112:115], v[168:175], v[176:183], v[112:115]
	v_mfma_f32_16x16x128_f8f6f4 v[104:107], v[160:167], v[184:191], v[104:107]
	v_mfma_f32_16x16x128_f8f6f4 v[96:99], v[168:175], v[184:191], v[96:99]
	v_mfma_f32_16x16x128_f8f6f4 v[88:91], v[160:167], v[192:199], v[88:91]
	v_mfma_f32_16x16x128_f8f6f4 v[80:83], v[168:175], v[192:199], v[80:83]
	v_mfma_f32_16x16x128_f8f6f4 v[72:75], v[160:167], v[200:207], v[72:75]
	v_mfma_f32_16x16x128_f8f6f4 v[64:67], v[168:175], v[200:207], v[64:67]
	s_setprio 0
	s_barrier
	s_add_u32 s26, s24, 0x80
	s_addc_u32 s27, s25, 0
	v_mov_b32_e32 v132, v134
	s_add_i32 s71, s71, s35
	ds_read_b128 v[176:179], v139 offset:49152
	ds_read_b128 v[180:183], v139 offset:50176
	ds_read_b128 v[184:187], v139 offset:51200
	ds_read_b128 v[188:191], v139 offset:52224
	ds_read_b128 v[192:195], v139 offset:53248
	ds_read_b128 v[196:199], v139 offset:54272
	ds_read_b128 v[200:203], v139 offset:55296
	ds_read_b128 v[204:207], v139 offset:56320
	s_mov_b32 m0, s71
	s_nop 0
	global_load_lds_dwordx4 v132, s[26:27]
	s_add_u32 s26, s24, 0x10080
	v_mov_b32_e32 v132, v134
	s_addc_u32 s27, s25, 0
	s_add_i32 m0, s71, 0x2000
	s_nop 0
	global_load_lds_dwordx4 v132, s[26:27]
	s_add_u32 s26, s24, 0x20080
	v_mov_b32_e32 v132, v134
	s_addc_u32 s27, s25, 0
	s_add_i32 s71, s74, s35
	s_mov_b32 m0, s71
	s_add_u32 s24, s24, 0x30080
	s_addc_u32 s25, s25, 0
	global_load_lds_dwordx4 v132, s[26:27]
	v_mov_b32_e32 v132, v134
	s_add_i32 m0, s71, 0x2000
	s_nop 0
	global_load_lds_dwordx4 v132, s[24:25]
	s_mov_b64 s[24:25], s[22:23]
	s_mov_b32 m0, s43
	s_nop 0
	global_load_lds_dwordx4 v133, s[24:25]
	s_mov_b32 m0, s44
	s_nop 0
	global_load_lds_dwordx4 v208, s[22:23]
	s_waitcnt vmcnt(8)
	s_waitcnt lgkmcnt(0)
	s_barrier
	s_setprio 3
	s_waitcnt lgkmcnt(0)
	v_mfma_f32_16x16x128_f8f6f4 v[60:63], v[144:151], v[176:183], v[60:63]
	v_mfma_f32_16x16x128_f8f6f4 v[52:55], v[152:159], v[176:183], v[52:55]
	v_mfma_f32_16x16x128_f8f6f4 v[44:47], v[144:151], v[184:191], v[44:47]
	v_mfma_f32_16x16x128_f8f6f4 v[36:39], v[152:159], v[184:191], v[36:39]
	v_mfma_f32_16x16x128_f8f6f4 v[28:31], v[144:151], v[192:199], v[28:31]
	v_mfma_f32_16x16x128_f8f6f4 v[20:23], v[152:159], v[192:199], v[20:23]
	v_mfma_f32_16x16x128_f8f6f4 v[12:15], v[144:151], v[200:207], v[12:15]
	v_mfma_f32_16x16x128_f8f6f4 v[4:7], v[152:159], v[200:207], v[4:7]
	v_mfma_f32_16x16x128_f8f6f4 v[56:59], v[160:167], v[176:183], v[56:59]
	v_mfma_f32_16x16x128_f8f6f4 v[48:51], v[168:175], v[176:183], v[48:51]
	v_mfma_f32_16x16x128_f8f6f4 v[40:43], v[160:167], v[184:191], v[40:43]
	v_mfma_f32_16x16x128_f8f6f4 v[32:35], v[168:175], v[184:191], v[32:35]
	v_mfma_f32_16x16x128_f8f6f4 v[24:27], v[160:167], v[192:199], v[24:27]
	v_mfma_f32_16x16x128_f8f6f4 v[16:19], v[168:175], v[192:199], v[16:19]
	v_mfma_f32_16x16x128_f8f6f4 v[8:11], v[160:167], v[200:207], v[8:11]
	v_mfma_f32_16x16x128_f8f6f4 v[0:3], v[168:175], v[200:207], v[0:3]
	s_setprio 0
	s_barrier
	s_add_i32 s70, s70, 2
	s_add_u32 s14, s14, 0x100
	s_addc_u32 s65, s65, 0
	s_add_u32 s68, s68, 0x100
	s_addc_u32 s69, s69, 0
	s_cmp_gt_u32 s70, 5
	s_cbranch_scc0 .LBB0_1124
	s_and_b64 vcc, exec, s[18:19]
	s_cbranch_vccz .LBB0_1127
	s_barrier

.LBB0_1286:
	ds_read_b128 v[72:75], v67
	ds_read_b128 v[76:79], v67 offset:1024
	ds_read_b128 v[80:83], v67 offset:2048
	ds_read_b128 v[84:87], v67 offset:3072
	ds_read_b128 v[88:91], v68
	ds_read_b128 v[92:95], v68 offset:1024
	ds_read_b128 v[96:99], v68 offset:2048
	ds_read_b128 v[100:103], v68 offset:3072
	s_cmp_eq_u32 s37, 4
	s_cselect_b32 s16, s8, s35
	s_cselect_b32 s17, s9, s36
	s_cselect_b32 s14, s0, s31
	s_cselect_b32 s15, s1, s34
	s_add_u32 s4, s16, 0x80
	s_addc_u32 s5, s17, 0
	ds_read_b128 v[104:107], v69
	ds_read_b128 v[108:111], v69 offset:1024
	ds_read_b128 v[112:115], v69 offset:2048
	ds_read_b128 v[116:119], v69 offset:3072
	ds_read_b128 v[120:123], v69 offset:4096
	ds_read_b128 v[124:127], v69 offset:5120
	ds_read_b128 v[128:131], v69 offset:6144
	ds_read_b128 v[132:135], v69 offset:7168
	s_waitcnt vmcnt(6)
	s_waitcnt lgkmcnt(0)
	s_barrier
	s_setprio 3
	s_waitcnt lgkmcnt(0)
	v_mfma_f32_16x16x128_f8f6f4 v[60:63], v[72:79], v[104:111], v[60:63]
	v_mfma_f32_16x16x128_f8f6f4 v[52:55], v[80:87], v[104:111], v[52:55]
	v_mfma_f32_16x16x128_f8f6f4 v[44:47], v[72:79], v[112:119], v[44:47]
	v_mfma_f32_16x16x128_f8f6f4 v[36:39], v[80:87], v[112:119], v[36:39]
	v_mfma_f32_16x16x128_f8f6f4 v[28:31], v[72:79], v[120:127], v[28:31]
	v_mfma_f32_16x16x128_f8f6f4 v[20:23], v[80:87], v[120:127], v[20:23]
	v_mfma_f32_16x16x128_f8f6f4 v[12:15], v[72:79], v[128:135], v[12:15]
	v_mfma_f32_16x16x128_f8f6f4 v[136:139], v[80:87], v[128:135], v[4:7]
	v_mfma_f32_16x16x128_f8f6f4 v[56:59], v[88:95], v[104:111], v[56:59]
	v_mfma_f32_16x16x128_f8f6f4 v[48:51], v[96:103], v[104:111], v[48:51]
	v_mfma_f32_16x16x128_f8f6f4 v[40:43], v[88:95], v[112:119], v[40:43]
	v_mfma_f32_16x16x128_f8f6f4 v[32:35], v[96:103], v[112:119], v[32:35]
	v_mfma_f32_16x16x128_f8f6f4 v[24:27], v[88:95], v[120:127], v[24:27]
	v_mfma_f32_16x16x128_f8f6f4 v[16:19], v[96:103], v[120:127], v[16:19]
	v_mfma_f32_16x16x128_f8f6f4 v[8:11], v[88:95], v[128:135], v[8:11]
	v_mfma_f32_16x16x128_f8f6f4 v[128:131], v[96:103], v[128:135], v[0:3]
	s_setprio 0
	s_barrier
	s_nop 4
	v_mov_b32_e32 v0, v64
	s_mov_b64 s[48:49], s[14:15]
	s_mov_b32 m0, s38
	s_nop 0
	global_load_lds_dwordx4 v0, s[48:49]
	s_add_u32 s48, s14, 0x10000
	v_mov_b32_e32 v0, v64
	s_addc_u32 s49, s15, 0
	s_mov_b32 m0, s39
	s_nop 0
	global_load_lds_dwordx4 v0, s[48:49]
	s_add_u32 s48, s14, 0x20000
	v_mov_b32_e32 v0, v64
	s_addc_u32 s49, s15, 0
	s_mov_b32 m0, s40
	s_nop 0
	global_load_lds_dwordx4 v0, s[48:49]
	v_mov_b32_e32 v0, v64
	s_add_u32 s48, s14, 0x30000
	s_addc_u32 s49, s15, 0
	s_mov_b32 m0, s41
	s_nop 0
	global_load_lds_dwordx4 v0, s[48:49]
	v_mov_b32_e32 v0, v65
	s_mov_b64 s[48:49], s[16:17]
	s_mov_b32 m0, s23
	s_nop 0
	global_load_lds_dwordx4 v0, s[48:49]
	v_mov_b32_e32 v0, v66
	s_mov_b32 m0, s25
	s_nop 0
	global_load_lds_dwordx4 v0, s[16:17]
	s_waitcnt vmcnt(6)
	s_waitcnt lgkmcnt(0)
	s_barrier
	s_barrier
	ds_read_b128 v[0:3], v70
	ds_read_b128 v[4:7], v70 offset:1024
	ds_read_b128 v[72:75], v70 offset:2048
	ds_read_b128 v[76:79], v70 offset:3072
	ds_read_b128 v[80:83], v71
	ds_read_b128 v[84:87], v71 offset:1024
	ds_read_b128 v[88:91], v71 offset:2048
	ds_read_b128 v[92:95], v71 offset:3072
	ds_read_b128 v[96:99], v69 offset:32768
	ds_read_b128 v[100:103], v69 offset:33792
	ds_read_b128 v[104:107], v69 offset:34816
	ds_read_b128 v[108:111], v69 offset:35840
	ds_read_b128 v[112:115], v69 offset:36864
	ds_read_b128 v[116:119], v69 offset:37888
	ds_read_b128 v[120:123], v69 offset:38912
	ds_read_b128 v[124:127], v69 offset:39936
	s_waitcnt vmcnt(6)
	s_waitcnt lgkmcnt(0)
	s_barrier
	s_setprio 3
	s_waitcnt lgkmcnt(0)
	v_mfma_f32_16x16x128_f8f6f4 v[60:63], v[0:7], v[96:103], v[60:63]
	v_mfma_f32_16x16x128_f8f6f4 v[52:55], v[72:79], v[96:103], v[52:55]
	v_mfma_f32_16x16x128_f8f6f4 v[44:47], v[0:7], v[104:111], v[44:47]
	v_mfma_f32_16x16x128_f8f6f4 v[36:39], v[72:79], v[104:111], v[36:39]
	v_mfma_f32_16x16x128_f8f6f4 v[28:31], v[0:7], v[112:119], v[28:31]
	v_mfma_f32_16x16x128_f8f6f4 v[20:23], v[72:79], v[112:119], v[20:23]
	v_mfma_f32_16x16x128_f8f6f4 v[12:15], v[0:7], v[120:127], v[12:15]
	v_mfma_f32_16x16x128_f8f6f4 v[4:7], v[72:79], v[120:127], v[136:139]
	v_mfma_f32_16x16x128_f8f6f4 v[56:59], v[80:87], v[96:103], v[56:59]
	s_add_u32 s16, s14, 0x80
	s_addc_u32 s17, s15, 0
	v_mfma_f32_16x16x128_f8f6f4 v[48:51], v[88:95], v[96:103], v[48:51]
	v_mfma_f32_16x16x128_f8f6f4 v[40:43], v[80:87], v[104:111], v[40:43]
	v_mfma_f32_16x16x128_f8f6f4 v[32:35], v[88:95], v[104:111], v[32:35]
	v_mfma_f32_16x16x128_f8f6f4 v[24:27], v[80:87], v[112:119], v[24:27]
	v_mfma_f32_16x16x128_f8f6f4 v[16:19], v[88:95], v[112:119], v[16:19]
	v_mfma_f32_16x16x128_f8f6f4 v[8:11], v[80:87], v[120:127], v[8:11]
	v_mfma_f32_16x16x128_f8f6f4 v[0:3], v[88:95], v[120:127], v[128:131]
	s_setprio 0
	s_barrier
	v_mov_b32_e32 v72, v64
	s_mov_b32 m0, s42
	s_nop 0
	global_load_lds_dwordx4 v72, s[16:17]
	s_add_u32 s16, s14, 0x10080
	v_mov_b32_e32 v72, v64
	s_addc_u32 s17, s15, 0
	s_mov_b32 m0, s43
	s_nop 0
	global_load_lds_dwordx4 v72, s[16:17]
	v_mov_b32_e32 v72, v64
	s_add_u32 s16, s14, 0x20080
	s_addc_u32 s17, s15, 0
	s_mov_b32 m0, s44
	s_add_u32 s14, s14, 0x30080
	global_load_lds_dwordx4 v72, s[16:17]
	v_mov_b32_e32 v72, v64
	s_addc_u32 s15, s15, 0
	s_mov_b32 m0, s45
	s_nop 0
	global_load_lds_dwordx4 v72, s[14:15]
	v_mov_b32_e32 v72, v65
	s_mov_b64 s[14:15], s[4:5]
	s_mov_b32 m0, s26
	s_nop 0
	global_load_lds_dwordx4 v72, s[14:15]
	v_mov_b32_e32 v72, v66
	s_mov_b32 m0, s27
	s_nop 0
	global_load_lds_dwordx4 v72, s[4:5]
	s_waitcnt vmcnt(6)
	s_waitcnt lgkmcnt(0)
	s_barrier
	s_barrier
	s_add_i32 s37, s37, 2
	s_add_u32 s31, s31, 0x100
	s_addc_u32 s34, s34, 0
	s_add_u32 s35, s35, 0x100
	s_addc_u32 s36, s36, 0
	s_cmp_gt_u32 s37, 5
	s_cbranch_scc0 .LBB0_1286
	s_cmpk_lt_u32 s22, 0x100
	s_cbranch_scc0 .LBB0_1289
	s_barrier

.LBB0_1402:
	s_waitcnt vmcnt(0)
	ds_read_b128 v[56:59], v197
	ds_read_b128 v[60:63], v197 offset:1024
	ds_read_b128 v[80:83], v197 offset:2048
	ds_read_b128 v[84:87], v197 offset:3072
	ds_read_b128 v[0:3], v198
	ds_read_b128 v[4:7], v198 offset:1024
	ds_read_b128 v[8:11], v198 offset:2048
	ds_read_b128 v[12:15], v198 offset:3072
	s_add_u32 s44, s36, 0x80
	s_addc_u32 s45, s37, 0
	s_add_u32 s48, s16, 0x80
	s_addc_u32 s49, s17, 0
	s_add_u32 s78, s42, 0x8080
	v_mov_b32_e32 v16, v195
	s_addc_u32 s79, s43, 0
	s_add_i32 m0, s52, 0xc000
	ds_read_b128 v[64:67], v199
	ds_read_b128 v[68:71], v199 offset:1024
	ds_read_b128 v[72:75], v199 offset:2048
	ds_read_b128 v[76:79], v199 offset:3072
	ds_read_b128 v[88:91], v199 offset:4096
	ds_read_b128 v[92:95], v199 offset:5120
	ds_read_b128 v[96:99], v199 offset:6144
	ds_read_b128 v[100:103], v199 offset:7168
	s_add_u32 s42, s42, 0xc080
	s_addc_u32 s43, s43, 0
	global_load_lds_dwordx4 v16, s[78:79] sc1
	v_mov_b32_e32 v16, v195
	s_add_i32 m0, s52, 0xe000
	s_nop 0
	global_load_lds_dwordx4 v16, s[42:43] sc1
	s_waitcnt vmcnt(8)
	s_waitcnt lgkmcnt(0)
	s_barrier
	s_setprio 3
	s_waitcnt lgkmcnt(0)
	v_mfma_f32_16x16x128_f8f6f4 v[16:19], v[56:63], v[64:71], 0
	v_mfma_f32_16x16x128_f8f6f4 v[20:23], v[80:87], v[64:71], 0
	v_mfma_f32_16x16x128_f8f6f4 v[24:27], v[56:63], v[72:79], 0
	v_mfma_f32_16x16x128_f8f6f4 v[28:31], v[80:87], v[72:79], 0
	v_mfma_f32_16x16x128_f8f6f4 v[32:35], v[56:63], v[88:95], 0
	v_mfma_f32_16x16x128_f8f6f4 v[36:39], v[80:87], v[88:95], 0
	v_mfma_f32_16x16x128_f8f6f4 v[40:43], v[56:63], v[96:103], 0
	v_mfma_f32_16x16x128_f8f6f4 v[44:47], v[80:87], v[96:103], 0
	v_mfma_f32_16x16x128_f8f6f4 v[48:51], v[0:7], v[64:71], 0
	v_mfma_f32_16x16x128_f8f6f4 v[52:55], v[8:15], v[64:71], 0
	v_mfma_f32_16x16x128_f8f6f4 v[64:67], v[0:7], v[72:79], 0
	v_mfma_f32_16x16x128_f8f6f4 v[68:71], v[8:15], v[72:79], 0
	v_mfma_f32_16x16x128_f8f6f4 v[72:75], v[0:7], v[88:95], 0
	v_mfma_f32_16x16x128_f8f6f4 v[76:79], v[8:15], v[88:95], 0
	v_mfma_f32_16x16x128_f8f6f4 v[128:131], v[0:7], v[96:103], 0
	v_mfma_f32_16x16x128_f8f6f4 v[132:135], v[8:15], v[96:103], 0
	s_setprio 0
	s_barrier
	v_mov_b32_e32 v120, v194
	s_mov_b64 s[42:43], s[16:17]
	s_add_i32 s21, s73, s51
	ds_read_b128 v[88:91], v199 offset:16384
	ds_read_b128 v[92:95], v199 offset:17408
	ds_read_b128 v[96:99], v199 offset:18432
	ds_read_b128 v[100:103], v199 offset:19456
	ds_read_b128 v[104:107], v199 offset:20480
	ds_read_b128 v[108:111], v199 offset:21504
	ds_read_b128 v[112:115], v199 offset:22528
	ds_read_b128 v[116:119], v199 offset:23552
	s_mov_b32 m0, s21
	s_nop 0
	global_load_lds_dwordx4 v120, s[42:43]
	s_add_u32 s42, s16, 0x4000
	v_mov_b32_e32 v120, v194
	s_addc_u32 s43, s17, 0
	s_add_i32 m0, s21, 0x2000
	s_nop 0
	global_load_lds_dwordx4 v120, s[42:43]
	s_add_u32 s42, s16, 0x8000
	v_mov_b32_e32 v120, v194
	s_addc_u32 s43, s17, 0
	s_add_i32 s21, s74, s51
	s_mov_b32 m0, s21
	s_nop 0
	global_load_lds_dwordx4 v120, s[42:43]
	s_add_u32 s42, s16, 0xc000
	v_mov_b32_e32 v120, v194
	s_addc_u32 s43, s17, 0
	s_add_i32 m0, s21, 0x2000
	s_nop 0
	global_load_lds_dwordx4 v120, s[42:43]
	v_mov_b32_e32 v120, v195
	s_mov_b64 s[42:43], s[36:37]
	s_mov_b32 m0, s52
	s_nop 0
	global_load_lds_dwordx4 v120, s[42:43] sc1
	s_add_u32 s42, s36, 0x4000
	v_mov_b32_e32 v120, v195
	s_addc_u32 s43, s37, 0
	s_mov_b32 m0, s53
	s_nop 0
	global_load_lds_dwordx4 v120, s[42:43] sc1
	s_waitcnt vmcnt(8)
	s_waitcnt lgkmcnt(0)
	s_barrier
	s_setprio 3
	s_waitcnt lgkmcnt(0)
	v_mfma_f32_16x16x128_f8f6f4 v[136:139], v[56:63], v[88:95], 0
	v_mfma_f32_16x16x128_f8f6f4 v[140:143], v[80:87], v[88:95], 0
	v_mfma_f32_16x16x128_f8f6f4 v[144:147], v[56:63], v[96:103], 0
	v_mfma_f32_16x16x128_f8f6f4 v[148:151], v[80:87], v[96:103], 0
	v_mfma_f32_16x16x128_f8f6f4 v[152:155], v[56:63], v[104:111], 0
	v_mfma_f32_16x16x128_f8f6f4 v[156:159], v[80:87], v[104:111], 0
	v_mfma_f32_16x16x128_f8f6f4 v[160:163], v[56:63], v[112:119], 0
	v_mfma_f32_16x16x128_f8f6f4 v[164:167], v[80:87], v[112:119], 0
	v_mfma_f32_16x16x128_f8f6f4 v[168:171], v[0:7], v[88:95], 0
	v_mfma_f32_16x16x128_f8f6f4 v[176:179], v[0:7], v[96:103], 0
	v_mfma_f32_16x16x128_f8f6f4 v[184:187], v[0:7], v[104:111], 0
	v_mfma_f32_16x16x128_f8f6f4 v[0:3], v[0:7], v[112:119], 0
	v_mfma_f32_16x16x128_f8f6f4 v[4:7], v[8:15], v[112:119], 0
	v_mfma_f32_16x16x128_f8f6f4 v[172:175], v[8:15], v[88:95], 0
	v_mfma_f32_16x16x128_f8f6f4 v[180:183], v[8:15], v[96:103], 0
	v_mfma_f32_16x16x128_f8f6f4 v[188:191], v[8:15], v[104:111], 0
	s_setprio 0
	s_barrier
	s_add_i32 s21, 0, 0x18000
	v_add_u32_e32 v56, s21, v196
	s_add_i32 s31, 0, 0x1c000
	ds_read_b128 v[8:11], v56
	ds_read_b128 v[12:15], v56 offset:1024
	ds_read_b128 v[200:203], v56 offset:2048
	ds_read_b128 v[204:207], v56 offset:3072
	v_add_u32_e32 v56, s31, v196
	ds_read_b128 v[208:211], v56
	ds_read_b128 v[212:215], v56 offset:1024
	ds_read_b128 v[216:219], v56 offset:2048
	ds_read_b128 v[220:223], v56 offset:3072
	s_add_u32 s42, s36, 0x8000
	v_mov_b32_e32 v56, v195
	s_addc_u32 s43, s37, 0
	s_mov_b32 m0, s60
	ds_read_b128 v[88:91], v199 offset:32768
	ds_read_b128 v[92:95], v199 offset:33792
	ds_read_b128 v[224:227], v199 offset:34816
	ds_read_b128 v[228:231], v199 offset:35840
	ds_read_b128 v[232:235], v199 offset:36864
	ds_read_b128 v[236:239], v199 offset:37888
	ds_read_b128 v[240:243], v199 offset:38912
	ds_read_b128 v[244:247], v199 offset:39936
	s_nop 0
	global_load_lds_dwordx4 v56, s[42:43] sc1
	s_add_u32 s42, s36, 0xc000
	v_mov_b32_e32 v56, v195
	s_addc_u32 s43, s37, 0
	s_mov_b32 m0, s61
	s_nop 0
	global_load_lds_dwordx4 v56, s[42:43] sc1
	s_waitcnt vmcnt(8)
	s_waitcnt lgkmcnt(0)
	s_barrier
	s_setprio 3
	s_waitcnt lgkmcnt(0)
	v_mfma_f32_16x16x128_f8f6f4 v[112:115], v[8:15], v[88:95], v[16:19]
	v_mfma_f32_16x16x128_f8f6f4 v[116:119], v[200:207], v[88:95], v[20:23]
	v_mfma_f32_16x16x128_f8f6f4 v[96:99], v[8:15], v[224:231], v[24:27]
	v_mfma_f32_16x16x128_f8f6f4 v[100:103], v[200:207], v[224:231], v[28:31]
	v_mfma_f32_16x16x128_f8f6f4 v[80:83], v[8:15], v[232:239], v[32:35]
	v_mfma_f32_16x16x128_f8f6f4 v[84:87], v[200:207], v[232:239], v[36:39]
	v_mfma_f32_16x16x128_f8f6f4 v[56:59], v[8:15], v[240:247], v[40:43]
	v_mfma_f32_16x16x128_f8f6f4 v[60:63], v[200:207], v[240:247], v[44:47]
	v_mfma_f32_16x16x128_f8f6f4 v[120:123], v[208:215], v[88:95], v[48:51]
	v_mfma_f32_16x16x128_f8f6f4 v[124:127], v[216:223], v[88:95], v[52:55]
	v_mfma_f32_16x16x128_f8f6f4 v[104:107], v[208:215], v[224:231], v[64:67]
	v_mfma_f32_16x16x128_f8f6f4 v[108:111], v[216:223], v[224:231], v[68:71]
	v_mfma_f32_16x16x128_f8f6f4 v[88:91], v[208:215], v[232:239], v[72:75]
	v_mfma_f32_16x16x128_f8f6f4 v[92:95], v[216:223], v[232:239], v[76:79]
	v_mfma_f32_16x16x128_f8f6f4 v[64:67], v[208:215], v[240:247], v[128:131]
	v_mfma_f32_16x16x128_f8f6f4 v[68:71], v[216:223], v[240:247], v[132:135]
	s_setprio 0
	s_barrier
	v_mov_b32_e32 v24, v194
	s_add_i32 s21, s21, s51
	ds_read_b128 v[16:19], v199 offset:49152
	ds_read_b128 v[20:23], v199 offset:50176
	ds_read_b128 v[128:131], v199 offset:51200
	ds_read_b128 v[132:135], v199 offset:52224
	ds_read_b128 v[224:227], v199 offset:53248
	ds_read_b128 v[228:231], v199 offset:54272
	ds_read_b128 v[232:235], v199 offset:55296
	ds_read_b128 v[236:239], v199 offset:56320
	s_mov_b32 m0, s21
	s_add_u32 s42, s16, 0x4080
	s_addc_u32 s43, s17, 0
	global_load_lds_dwordx4 v24, s[48:49]
	v_mov_b32_e32 v24, v194
	s_add_i32 m0, s21, 0x2000
	s_nop 0
	global_load_lds_dwordx4 v24, s[42:43]
	s_add_u32 s42, s16, 0x8080
	v_mov_b32_e32 v24, v194
	s_addc_u32 s43, s17, 0
	s_add_i32 s21, s31, s51
	s_mov_b32 m0, s21
	s_nop 0
	global_load_lds_dwordx4 v24, s[42:43]
	v_mov_b32_e32 v24, v194
	s_add_u32 s42, s16, 0xc080
	s_addc_u32 s43, s17, 0
	s_add_i32 m0, s21, 0x2000
	s_nop 0
	global_load_lds_dwordx4 v24, s[42:43]
	v_mov_b32_e32 v24, v195
	s_mov_b32 m0, s68
	s_add_u32 s42, s36, 0x4080
	s_addc_u32 s43, s37, 0
	global_load_lds_dwordx4 v24, s[44:45] sc1
	v_mov_b32_e32 v24, v195
	s_mov_b32 m0, s69
	s_nop 0
	global_load_lds_dwordx4 v24, s[42:43] sc1
	s_waitcnt vmcnt(8)
	s_waitcnt lgkmcnt(0)
	s_barrier
	s_setprio 3
	s_waitcnt lgkmcnt(0)
	v_mfma_f32_16x16x128_f8f6f4 v[48:51], v[8:15], v[16:23], v[136:139]
	v_mfma_f32_16x16x128_f8f6f4 v[52:55], v[200:207], v[16:23], v[140:143]
	v_mfma_f32_16x16x128_f8f6f4 v[32:35], v[8:15], v[128:135], v[144:147]
	v_mfma_f32_16x16x128_f8f6f4 v[36:39], v[200:207], v[128:135], v[148:151]
	v_mfma_f32_16x16x128_f8f6f4 v[24:27], v[8:15], v[224:231], v[152:155]
	v_mfma_f32_16x16x128_f8f6f4 v[28:31], v[200:207], v[224:231], v[156:159]
	v_mfma_f32_16x16x128_f8f6f4 v[8:11], v[8:15], v[232:239], v[160:163]
	v_mfma_f32_16x16x128_f8f6f4 v[12:15], v[200:207], v[232:239], v[164:167]
	v_mfma_f32_16x16x128_f8f6f4 v[72:75], v[208:215], v[16:23], v[168:171]
	v_mfma_f32_16x16x128_f8f6f4 v[76:79], v[216:223], v[16:23], v[172:175]
	v_mfma_f32_16x16x128_f8f6f4 v[40:43], v[208:215], v[128:135], v[176:179]
	v_mfma_f32_16x16x128_f8f6f4 v[44:47], v[216:223], v[128:135], v[180:183]
	v_mfma_f32_16x16x128_f8f6f4 v[16:19], v[208:215], v[224:231], v[184:187]
	v_mfma_f32_16x16x128_f8f6f4 v[20:23], v[216:223], v[224:231], v[188:191]
	v_mfma_f32_16x16x128_f8f6f4 v[0:3], v[208:215], v[232:239], v[0:3]
	v_mfma_f32_16x16x128_f8f6f4 v[4:7], v[216:223], v[232:239], v[4:7]
	s_setprio 0
	s_barrier
	s_andn2_b64 vcc, exec, s[24:25]
	s_cbranch_vccnz .LBB0_1404
	s_barrier

.LBB0_1769:
	ds_read_b128 v[56:59], v155
	ds_read_b128 v[60:63], v155 offset:1024
	ds_read_b128 v[68:71], v155 offset:2048
	ds_read_b128 v[76:79], v155 offset:3072
	ds_read_b128 v[146:149], v156
	ds_read_b128 v[160:163], v156 offset:1024
	ds_read_b128 v[164:167], v156 offset:2048
	ds_read_b128 v[168:171], v156 offset:3072
	s_add_u32 s69, s6, 0xfffa0080
	s_addc_u32 s70, s7, -1
	s_cmp_eq_u32 s53, 12
	s_cselect_b32 s71, s61, s70
	s_cselect_b32 s70, s60, s69
	s_cselect_b32 s74, s64, s5
	s_cselect_b32 s75, s65, s51
	s_add_u32 s72, s70, 0x80
	s_addc_u32 s73, s71, 0
	s_add_u32 s80, s6, 0xfffe0000
	v_mov_b32_e32 v150, v153
	s_addc_u32 s81, s7, -1
	ds_read_b128 v[172:175], v157
	ds_read_b128 v[176:179], v157 offset:1024
	ds_read_b128 v[180:183], v157 offset:2048
	ds_read_b128 v[184:187], v157 offset:3072
	ds_read_b128 v[188:191], v157 offset:4096
	ds_read_b128 v[192:195], v157 offset:5120
	ds_read_b128 v[196:199], v157 offset:6144
	ds_read_b128 v[200:203], v157 offset:7168
	s_add_i32 m0, s25, 0xc000
	s_nop 0
	global_load_lds_dwordx4 v150, s[80:81]
	v_mov_b32_e32 v150, v153
	s_mov_b64 s[80:81], s[6:7]
	s_add_i32 m0, s25, 0xe000
	s_nop 0
	global_load_lds_dwordx4 v150, s[80:81]
	s_waitcnt vmcnt(8)
	s_waitcnt lgkmcnt(0)
	s_barrier
	s_setprio 3
	s_waitcnt lgkmcnt(0)
	v_mfma_f32_16x16x32_bf16 v[140:143], v[56:59], v[172:175], v[140:143]
	v_mfma_f32_16x16x32_bf16 v[136:139], v[68:71], v[172:175], v[136:139]
	v_mfma_f32_16x16x32_bf16 v[124:127], v[56:59], v[180:183], v[124:127]
	v_mfma_f32_16x16x32_bf16 v[120:123], v[68:71], v[180:183], v[120:123]
	v_mfma_f32_16x16x32_bf16 v[108:111], v[56:59], v[188:191], v[108:111]
	v_mfma_f32_16x16x32_bf16 v[104:107], v[68:71], v[188:191], v[104:107]
	v_mfma_f32_16x16x32_bf16 v[92:95], v[56:59], v[196:199], v[92:95]
	v_mfma_f32_16x16x32_bf16 v[88:91], v[68:71], v[196:199], v[88:91]
	v_mfma_f32_16x16x32_bf16 v[140:143], v[60:63], v[176:179], v[140:143]
	v_mfma_f32_16x16x32_bf16 v[136:139], v[76:79], v[176:179], v[136:139]
	v_mfma_f32_16x16x32_bf16 v[124:127], v[60:63], v[184:187], v[124:127]
	v_mfma_f32_16x16x32_bf16 v[120:123], v[76:79], v[184:187], v[120:123]
	v_mfma_f32_16x16x32_bf16 v[108:111], v[60:63], v[192:195], v[108:111]
	v_mfma_f32_16x16x32_bf16 v[104:107], v[76:79], v[192:195], v[104:107]
	v_mfma_f32_16x16x32_bf16 v[92:95], v[60:63], v[200:203], v[92:95]
	v_mfma_f32_16x16x32_bf16 v[88:91], v[76:79], v[200:203], v[88:91]
	v_mfma_f32_16x16x32_bf16 v[132:135], v[146:149], v[172:175], v[132:135]
	v_mfma_f32_16x16x32_bf16 v[128:131], v[164:167], v[172:175], v[128:131]
	v_mfma_f32_16x16x32_bf16 v[116:119], v[146:149], v[180:183], v[116:119]
	v_mfma_f32_16x16x32_bf16 v[112:115], v[164:167], v[180:183], v[112:115]
	v_mfma_f32_16x16x32_bf16 v[100:103], v[146:149], v[188:191], v[100:103]
	v_mfma_f32_16x16x32_bf16 v[96:99], v[164:167], v[188:191], v[96:99]
	v_mfma_f32_16x16x32_bf16 v[84:87], v[146:149], v[196:199], v[84:87]
	v_mfma_f32_16x16x32_bf16 v[80:83], v[164:167], v[196:199], v[80:83]
	v_mfma_f32_16x16x32_bf16 v[132:135], v[160:163], v[176:179], v[132:135]
	v_mfma_f32_16x16x32_bf16 v[128:131], v[168:171], v[176:179], v[128:131]
	v_mfma_f32_16x16x32_bf16 v[116:119], v[160:163], v[184:187], v[116:119]
	v_mfma_f32_16x16x32_bf16 v[112:115], v[168:171], v[184:187], v[112:115]
	v_mfma_f32_16x16x32_bf16 v[100:103], v[160:163], v[192:195], v[100:103]
	v_mfma_f32_16x16x32_bf16 v[96:99], v[168:171], v[192:195], v[96:99]
	v_mfma_f32_16x16x32_bf16 v[84:87], v[160:163], v[200:203], v[84:87]
	v_mfma_f32_16x16x32_bf16 v[80:83], v[168:171], v[200:203], v[80:83]
	s_setprio 0
	s_barrier
	v_mov_b32_e32 v150, v152
	s_mov_b64 s[80:81], s[74:75]
	s_add_i32 s69, s49, s23
	ds_read_b128 v[172:175], v157 offset:16384
	ds_read_b128 v[176:179], v157 offset:17408
	ds_read_b128 v[180:183], v157 offset:18432
	ds_read_b128 v[184:187], v157 offset:19456
	ds_read_b128 v[188:191], v157 offset:20480
	ds_read_b128 v[192:195], v157 offset:21504
	ds_read_b128 v[196:199], v157 offset:22528
	ds_read_b128 v[200:203], v157 offset:23552
	s_mov_b32 m0, s69
	s_nop 0
	global_load_lds_dwordx4 v150, s[80:81]
	s_add_u32 s80, s74, 0x20000
	v_mov_b32_e32 v150, v152
	s_addc_u32 s81, s75, 0
	s_add_i32 m0, s69, 0x2000
	s_nop 0
	global_load_lds_dwordx4 v150, s[80:81]
	s_add_u32 s80, s74, 0x40000
	v_mov_b32_e32 v150, v152
	s_addc_u32 s81, s75, 0
	s_add_i32 s69, s77, s23
	s_mov_b32 m0, s69
	s_nop 0
	global_load_lds_dwordx4 v150, s[80:81]
	s_add_u32 s80, s74, 0x60000
	v_mov_b32_e32 v150, v152
	s_addc_u32 s81, s75, 0
	s_add_i32 m0, s69, 0x2000
	s_nop 0
	global_load_lds_dwordx4 v150, s[80:81]
	v_mov_b32_e32 v150, v153
	s_mov_b64 s[80:81], s[70:71]
	s_mov_b32 m0, s25
	s_nop 0
	global_load_lds_dwordx4 v150, s[80:81]
	s_add_u32 s80, s70, 0x20000
	v_mov_b32_e32 v150, v153
	s_addc_u32 s81, s71, 0
	s_mov_b32 m0, s27
	s_nop 0
	global_load_lds_dwordx4 v150, s[80:81]
	s_waitcnt vmcnt(8)
	s_waitcnt lgkmcnt(0)
	s_barrier
	s_setprio 3
	s_waitcnt lgkmcnt(0)
	v_mfma_f32_16x16x32_bf16 v[72:75], v[56:59], v[172:175], v[72:75]
	v_mfma_f32_16x16x32_bf16 v[64:67], v[68:71], v[172:175], v[64:67]
	v_mfma_f32_16x16x32_bf16 v[44:47], v[56:59], v[180:183], v[44:47]
	v_mfma_f32_16x16x32_bf16 v[40:43], v[68:71], v[180:183], v[40:43]
	v_mfma_f32_16x16x32_bf16 v[28:31], v[56:59], v[188:191], v[28:31]
	v_mfma_f32_16x16x32_bf16 v[24:27], v[68:71], v[188:191], v[24:27]
	v_mfma_f32_16x16x32_bf16 v[12:15], v[56:59], v[196:199], v[12:15]
	v_mfma_f32_16x16x32_bf16 v[8:11], v[68:71], v[196:199], v[8:11]
	v_mfma_f32_16x16x32_bf16 v[72:75], v[60:63], v[176:179], v[72:75]
	v_mfma_f32_16x16x32_bf16 v[64:67], v[76:79], v[176:179], v[64:67]
	v_mfma_f32_16x16x32_bf16 v[44:47], v[60:63], v[184:187], v[44:47]
	v_mfma_f32_16x16x32_bf16 v[40:43], v[76:79], v[184:187], v[40:43]
	v_mfma_f32_16x16x32_bf16 v[28:31], v[60:63], v[192:195], v[28:31]
	v_mfma_f32_16x16x32_bf16 v[24:27], v[76:79], v[192:195], v[24:27]
	v_mfma_f32_16x16x32_bf16 v[12:15], v[60:63], v[200:203], v[12:15]
	v_mfma_f32_16x16x32_bf16 v[8:11], v[76:79], v[200:203], v[8:11]
	v_mfma_f32_16x16x32_bf16 v[52:55], v[146:149], v[172:175], v[52:55]
	v_mfma_f32_16x16x32_bf16 v[48:51], v[164:167], v[172:175], v[48:51]
	v_mfma_f32_16x16x32_bf16 v[36:39], v[146:149], v[180:183], v[36:39]
	v_mfma_f32_16x16x32_bf16 v[32:35], v[164:167], v[180:183], v[32:35]
	v_mfma_f32_16x16x32_bf16 v[20:23], v[146:149], v[188:191], v[20:23]
	v_mfma_f32_16x16x32_bf16 v[16:19], v[164:167], v[188:191], v[16:19]
	v_mfma_f32_16x16x32_bf16 v[4:7], v[146:149], v[196:199], v[4:7]
	v_mfma_f32_16x16x32_bf16 v[0:3], v[164:167], v[196:199], v[0:3]
	v_mfma_f32_16x16x32_bf16 v[52:55], v[160:163], v[176:179], v[52:55]
	v_mfma_f32_16x16x32_bf16 v[48:51], v[168:171], v[176:179], v[48:51]
	v_mfma_f32_16x16x32_bf16 v[36:39], v[160:163], v[184:187], v[36:39]
	v_mfma_f32_16x16x32_bf16 v[32:35], v[168:171], v[184:187], v[32:35]
	v_mfma_f32_16x16x32_bf16 v[20:23], v[160:163], v[192:195], v[20:23]
	v_mfma_f32_16x16x32_bf16 v[16:19], v[168:171], v[192:195], v[16:19]
	v_mfma_f32_16x16x32_bf16 v[4:7], v[160:163], v[200:203], v[4:7]
	v_mfma_f32_16x16x32_bf16 v[0:3], v[168:171], v[200:203], v[0:3]
	s_setprio 0
	s_barrier
	s_add_i32 s69, 0, 0x18000
	s_add_i32 s82, 0, 0x1c000
	v_add_u32_e32 v76, s69, v154
	v_add_u32_e32 v150, s82, v154
	ds_read_b128 v[56:59], v76
	ds_read_b128 v[60:63], v76 offset:1024
	ds_read_b128 v[68:71], v76 offset:2048
	ds_read_b128 v[76:79], v76 offset:3072
	ds_read_b128 v[146:149], v150
	ds_read_b128 v[160:163], v150 offset:1024
	ds_read_b128 v[164:167], v150 offset:2048
	ds_read_b128 v[168:171], v150 offset:3072
	s_add_u32 s80, s70, 0x40000
	v_mov_b32_e32 v150, v153
	s_addc_u32 s81, s71, 0
	s_mov_b32 m0, s29
	ds_read_b128 v[172:175], v157 offset:32768
	ds_read_b128 v[176:179], v157 offset:33792
	ds_read_b128 v[180:183], v157 offset:34816
	ds_read_b128 v[184:187], v157 offset:35840
	ds_read_b128 v[188:191], v157 offset:36864
	ds_read_b128 v[192:195], v157 offset:37888
	ds_read_b128 v[196:199], v157 offset:38912
	ds_read_b128 v[200:203], v157 offset:39936
	s_nop 0
	global_load_lds_dwordx4 v150, s[80:81]
	s_add_u32 s80, s70, 0x60000
	v_mov_b32_e32 v150, v153
	s_addc_u32 s81, s71, 0
	s_mov_b32 m0, s31
	s_nop 0
	global_load_lds_dwordx4 v150, s[80:81]
	s_waitcnt vmcnt(8)
	s_waitcnt lgkmcnt(0)
	s_barrier
	s_setprio 3
	s_waitcnt lgkmcnt(0)
	v_mfma_f32_16x16x32_bf16 v[140:143], v[56:59], v[172:175], v[140:143]
	v_mfma_f32_16x16x32_bf16 v[136:139], v[68:71], v[172:175], v[136:139]
	v_mfma_f32_16x16x32_bf16 v[124:127], v[56:59], v[180:183], v[124:127]
	v_mfma_f32_16x16x32_bf16 v[120:123], v[68:71], v[180:183], v[120:123]
	v_mfma_f32_16x16x32_bf16 v[108:111], v[56:59], v[188:191], v[108:111]
	v_mfma_f32_16x16x32_bf16 v[104:107], v[68:71], v[188:191], v[104:107]
	v_mfma_f32_16x16x32_bf16 v[92:95], v[56:59], v[196:199], v[92:95]
	v_mfma_f32_16x16x32_bf16 v[88:91], v[68:71], v[196:199], v[88:91]
	v_mfma_f32_16x16x32_bf16 v[140:143], v[60:63], v[176:179], v[140:143]
	v_mfma_f32_16x16x32_bf16 v[136:139], v[76:79], v[176:179], v[136:139]
	v_mfma_f32_16x16x32_bf16 v[124:127], v[60:63], v[184:187], v[124:127]
	v_mfma_f32_16x16x32_bf16 v[120:123], v[76:79], v[184:187], v[120:123]
	v_mfma_f32_16x16x32_bf16 v[108:111], v[60:63], v[192:195], v[108:111]
	v_mfma_f32_16x16x32_bf16 v[104:107], v[76:79], v[192:195], v[104:107]
	v_mfma_f32_16x16x32_bf16 v[92:95], v[60:63], v[200:203], v[92:95]
	v_mfma_f32_16x16x32_bf16 v[88:91], v[76:79], v[200:203], v[88:91]
	v_mfma_f32_16x16x32_bf16 v[132:135], v[146:149], v[172:175], v[132:135]
	v_mfma_f32_16x16x32_bf16 v[128:131], v[164:167], v[172:175], v[128:131]
	v_mfma_f32_16x16x32_bf16 v[116:119], v[146:149], v[180:183], v[116:119]
	v_mfma_f32_16x16x32_bf16 v[112:115], v[164:167], v[180:183], v[112:115]
	v_mfma_f32_16x16x32_bf16 v[100:103], v[146:149], v[188:191], v[100:103]
	v_mfma_f32_16x16x32_bf16 v[96:99], v[164:167], v[188:191], v[96:99]
	v_mfma_f32_16x16x32_bf16 v[84:87], v[146:149], v[196:199], v[84:87]
	v_mfma_f32_16x16x32_bf16 v[80:83], v[164:167], v[196:199], v[80:83]
	v_mfma_f32_16x16x32_bf16 v[132:135], v[160:163], v[176:179], v[132:135]
	v_mfma_f32_16x16x32_bf16 v[128:131], v[168:171], v[176:179], v[128:131]
	v_mfma_f32_16x16x32_bf16 v[116:119], v[160:163], v[184:187], v[116:119]
	v_mfma_f32_16x16x32_bf16 v[112:115], v[168:171], v[184:187], v[112:115]
	v_mfma_f32_16x16x32_bf16 v[100:103], v[160:163], v[192:195], v[100:103]
	v_mfma_f32_16x16x32_bf16 v[96:99], v[168:171], v[192:195], v[96:99]
	v_mfma_f32_16x16x32_bf16 v[84:87], v[160:163], v[200:203], v[84:87]
	v_mfma_f32_16x16x32_bf16 v[80:83], v[168:171], v[200:203], v[80:83]
	s_setprio 0
	s_barrier
	s_add_u32 s80, s74, 0x80
	s_addc_u32 s81, s75, 0
	v_mov_b32_e32 v150, v152
	s_add_i32 s69, s69, s23
	ds_read_b128 v[172:175], v157 offset:49152
	ds_read_b128 v[176:179], v157 offset:50176
	ds_read_b128 v[180:183], v157 offset:51200
	ds_read_b128 v[184:187], v157 offset:52224
	ds_read_b128 v[188:191], v157 offset:53248
	ds_read_b128 v[192:195], v157 offset:54272
	ds_read_b128 v[196:199], v157 offset:55296
	ds_read_b128 v[200:203], v157 offset:56320
	s_mov_b32 m0, s69
	s_nop 0
	global_load_lds_dwordx4 v150, s[80:81]
	s_add_u32 s80, s74, 0x20080
	v_mov_b32_e32 v150, v152
	s_addc_u32 s81, s75, 0
	s_add_i32 m0, s69, 0x2000
	s_nop 0
	global_load_lds_dwordx4 v150, s[80:81]
	s_add_u32 s80, s74, 0x40080
	v_mov_b32_e32 v150, v152
	s_addc_u32 s81, s75, 0
	s_add_i32 s69, s82, s23
	s_mov_b32 m0, s69
	s_add_u32 s74, s74, 0x60080
	global_load_lds_dwordx4 v150, s[80:81]
	v_mov_b32_e32 v150, v152
	s_addc_u32 s75, s75, 0
	s_add_i32 m0, s69, 0x2000
	s_add_u32 s70, s70, 0x20080
	global_load_lds_dwordx4 v150, s[74:75]
	v_mov_b32_e32 v150, v153
	s_mov_b32 m0, s43
	s_addc_u32 s71, s71, 0
	global_load_lds_dwordx4 v150, s[72:73]
	v_mov_b32_e32 v150, v153
	s_mov_b32 m0, s45
	s_nop 0
	global_load_lds_dwordx4 v150, s[70:71]
	s_waitcnt vmcnt(8)
	s_waitcnt lgkmcnt(0)
	s_barrier
	s_setprio 3
	s_waitcnt lgkmcnt(0)
	v_mfma_f32_16x16x32_bf16 v[72:75], v[56:59], v[172:175], v[72:75]
	v_mfma_f32_16x16x32_bf16 v[64:67], v[68:71], v[172:175], v[64:67]
	v_mfma_f32_16x16x32_bf16 v[44:47], v[56:59], v[180:183], v[44:47]
	v_mfma_f32_16x16x32_bf16 v[40:43], v[68:71], v[180:183], v[40:43]
	v_mfma_f32_16x16x32_bf16 v[28:31], v[56:59], v[188:191], v[28:31]
	v_mfma_f32_16x16x32_bf16 v[24:27], v[68:71], v[188:191], v[24:27]
	v_mfma_f32_16x16x32_bf16 v[12:15], v[56:59], v[196:199], v[12:15]
	v_mfma_f32_16x16x32_bf16 v[8:11], v[68:71], v[196:199], v[8:11]
	v_mfma_f32_16x16x32_bf16 v[72:75], v[60:63], v[176:179], v[72:75]
	v_mfma_f32_16x16x32_bf16 v[64:67], v[76:79], v[176:179], v[64:67]
	v_mfma_f32_16x16x32_bf16 v[44:47], v[60:63], v[184:187], v[44:47]
	v_mfma_f32_16x16x32_bf16 v[40:43], v[76:79], v[184:187], v[40:43]
	v_mfma_f32_16x16x32_bf16 v[28:31], v[60:63], v[192:195], v[28:31]
	v_mfma_f32_16x16x32_bf16 v[24:27], v[76:79], v[192:195], v[24:27]
	v_mfma_f32_16x16x32_bf16 v[12:15], v[60:63], v[200:203], v[12:15]
	v_mfma_f32_16x16x32_bf16 v[8:11], v[76:79], v[200:203], v[8:11]
	v_mfma_f32_16x16x32_bf16 v[52:55], v[146:149], v[172:175], v[52:55]
	v_mfma_f32_16x16x32_bf16 v[48:51], v[164:167], v[172:175], v[48:51]
	v_mfma_f32_16x16x32_bf16 v[36:39], v[146:149], v[180:183], v[36:39]
	v_mfma_f32_16x16x32_bf16 v[32:35], v[164:167], v[180:183], v[32:35]
	v_mfma_f32_16x16x32_bf16 v[20:23], v[146:149], v[188:191], v[20:23]
	v_mfma_f32_16x16x32_bf16 v[16:19], v[164:167], v[188:191], v[16:19]
	v_mfma_f32_16x16x32_bf16 v[4:7], v[146:149], v[196:199], v[4:7]
	v_mfma_f32_16x16x32_bf16 v[0:3], v[164:167], v[196:199], v[0:3]
	v_mfma_f32_16x16x32_bf16 v[52:55], v[160:163], v[176:179], v[52:55]
	v_mfma_f32_16x16x32_bf16 v[48:51], v[168:171], v[176:179], v[48:51]
	v_mfma_f32_16x16x32_bf16 v[36:39], v[160:163], v[184:187], v[36:39]
	v_mfma_f32_16x16x32_bf16 v[32:35], v[168:171], v[184:187], v[32:35]
	v_mfma_f32_16x16x32_bf16 v[20:23], v[160:163], v[192:195], v[20:23]
	v_mfma_f32_16x16x32_bf16 v[16:19], v[168:171], v[192:195], v[16:19]
	v_mfma_f32_16x16x32_bf16 v[4:7], v[160:163], v[200:203], v[4:7]
	v_mfma_f32_16x16x32_bf16 v[0:3], v[168:171], v[200:203], v[0:3]
	s_setprio 0
	s_barrier
	s_add_i32 s53, s53, 2
	s_add_u32 s5, s5, 0x100
	s_addc_u32 s51, s51, 0
	s_add_u32 s6, s6, 0x100
	s_addc_u32 s7, s7, 0
	s_cmp_gt_u32 s53, 13
	s_cbranch_scc0 .LBB0_1769
	s_mov_b64 s[46:47], s[94:95]
	s_and_b64 vcc, exec, s[18:19]
	s_cbranch_vccz .LBB0_1772
	s_barrier

.LBB0_2137:
	ds_read_b128 v[8:11], v177
	ds_read_b128 v[12:15], v177 offset:1024
	ds_read_b128 v[136:139], v177 offset:2048
	ds_read_b128 v[140:143], v177 offset:3072
	ds_read_b128 v[146:149], v178
	ds_read_b128 v[150:153], v178 offset:1024
	ds_read_b128 v[154:157], v178 offset:2048
	ds_read_b128 v[158:161], v178 offset:3072
	s_add_u32 s30, s28, 0xfffa0080
	s_addc_u32 s31, s29, -1
	s_cmp_eq_u32 s65, 12
	s_cselect_b32 s30, s22, s30
	s_cselect_b32 s31, s23, s31
	s_cselect_b32 s36, s24, s19
	s_cselect_b32 s37, s25, s21
	s_add_u32 s34, s30, 0x80
	s_addc_u32 s35, s31, 0
	s_add_u32 s68, s28, 0xfffe0000
	v_mov_b32_e32 v170, v175
	s_addc_u32 s69, s29, -1
	ds_read_b128 v[162:165], v179
	ds_read_b128 v[166:169], v179 offset:1024
	ds_read_b128 v[180:183], v179 offset:2048
	ds_read_b128 v[184:187], v179 offset:3072
	ds_read_b128 v[188:191], v179 offset:4096
	ds_read_b128 v[192:195], v179 offset:5120
	ds_read_b128 v[196:199], v179 offset:6144
	ds_read_b128 v[200:203], v179 offset:7168
	s_add_i32 m0, s27, 0xc000
	s_nop 0
	global_load_lds_dwordx4 v170, s[68:69]
	v_mov_b32_e32 v170, v175
	s_mov_b64 s[68:69], s[28:29]
	s_add_i32 m0, s27, 0xe000
	s_nop 0
	global_load_lds_dwordx4 v170, s[68:69]
	s_waitcnt vmcnt(8)
	s_waitcnt lgkmcnt(0)
	s_barrier
	s_setprio 3
	s_waitcnt lgkmcnt(0)
	v_mfma_f32_16x16x128_f8f6f4 v[132:135], v[8:15], v[162:169], v[132:135]
	v_mfma_f32_16x16x128_f8f6f4 v[128:131], v[136:143], v[162:169], v[128:131]
	v_mfma_f32_16x16x128_f8f6f4 v[116:119], v[8:15], v[180:187], v[116:119]
	v_mfma_f32_16x16x128_f8f6f4 v[112:115], v[136:143], v[180:187], v[112:115]
	v_mfma_f32_16x16x128_f8f6f4 v[100:103], v[8:15], v[188:195], v[100:103]
	v_mfma_f32_16x16x128_f8f6f4 v[96:99], v[136:143], v[188:195], v[96:99]
	v_mfma_f32_16x16x128_f8f6f4 v[84:87], v[8:15], v[196:203], v[84:87]
	v_mfma_f32_16x16x128_f8f6f4 v[80:83], v[136:143], v[196:203], v[80:83]
	v_mfma_f32_16x16x128_f8f6f4 v[124:127], v[146:153], v[162:169], v[124:127]
	v_mfma_f32_16x16x128_f8f6f4 v[120:123], v[154:161], v[162:169], v[120:123]
	v_mfma_f32_16x16x128_f8f6f4 v[108:111], v[146:153], v[180:187], v[108:111]
	v_mfma_f32_16x16x128_f8f6f4 v[104:107], v[154:161], v[180:187], v[104:107]
	v_mfma_f32_16x16x128_f8f6f4 v[92:95], v[146:153], v[188:195], v[92:95]
	v_mfma_f32_16x16x128_f8f6f4 v[88:91], v[154:161], v[188:195], v[88:91]
	v_mfma_f32_16x16x128_f8f6f4 v[76:79], v[146:153], v[196:203], v[76:79]
	v_mfma_f32_16x16x128_f8f6f4 v[72:75], v[154:161], v[196:203], v[72:75]
	s_setprio 0
	s_barrier
	v_mov_b32_e32 v170, v174
	s_mov_b64 s[68:69], s[36:37]
	s_add_i32 s70, s60, s39
	ds_read_b128 v[162:165], v179 offset:16384
	ds_read_b128 v[166:169], v179 offset:17408
	ds_read_b128 v[180:183], v179 offset:18432
	ds_read_b128 v[184:187], v179 offset:19456
	ds_read_b128 v[188:191], v179 offset:20480
	ds_read_b128 v[192:195], v179 offset:21504
	ds_read_b128 v[196:199], v179 offset:22528
	ds_read_b128 v[200:203], v179 offset:23552
	s_mov_b32 m0, s70
	s_nop 0
	global_load_lds_dwordx4 v170, s[68:69]
	s_add_u32 s68, s36, 0x20000
	v_mov_b32_e32 v170, v174
	s_addc_u32 s69, s37, 0
	s_add_i32 m0, s70, 0x2000
	s_nop 0
	global_load_lds_dwordx4 v170, s[68:69]
	s_add_u32 s68, s36, 0x40000
	v_mov_b32_e32 v170, v174
	s_addc_u32 s69, s37, 0
	s_add_i32 s70, s61, s39
	s_mov_b32 m0, s70
	s_nop 0
	global_load_lds_dwordx4 v170, s[68:69]
	s_add_u32 s68, s36, 0x60000
	v_mov_b32_e32 v170, v174
	s_addc_u32 s69, s37, 0
	s_add_i32 m0, s70, 0x2000
	s_nop 0
	global_load_lds_dwordx4 v170, s[68:69]
	v_mov_b32_e32 v170, v175
	s_mov_b64 s[68:69], s[30:31]
	s_mov_b32 m0, s27
	s_nop 0
	global_load_lds_dwordx4 v170, s[68:69]
	s_add_u32 s68, s30, 0x20000
	v_mov_b32_e32 v170, v175
	s_addc_u32 s69, s31, 0
	s_mov_b32 m0, s41
	s_nop 0
	global_load_lds_dwordx4 v170, s[68:69]
	s_waitcnt vmcnt(8)
	s_waitcnt lgkmcnt(0)
	s_barrier
	s_setprio 3
	s_waitcnt lgkmcnt(0)
	v_mfma_f32_16x16x128_f8f6f4 v[68:71], v[8:15], v[162:169], v[68:71]
	v_mfma_f32_16x16x128_f8f6f4 v[64:67], v[136:143], v[162:169], v[64:67]
	v_mfma_f32_16x16x128_f8f6f4 v[52:55], v[8:15], v[180:187], v[52:55]
	v_mfma_f32_16x16x128_f8f6f4 v[48:51], v[136:143], v[180:187], v[48:51]
	v_mfma_f32_16x16x128_f8f6f4 v[36:39], v[8:15], v[188:195], v[36:39]
	v_mfma_f32_16x16x128_f8f6f4 v[32:35], v[136:143], v[188:195], v[32:35]
	v_mfma_f32_16x16x128_f8f6f4 v[20:23], v[8:15], v[196:203], v[20:23]
	v_mfma_f32_16x16x128_f8f6f4 v[16:19], v[136:143], v[196:203], v[16:19]
	v_mfma_f32_16x16x128_f8f6f4 v[60:63], v[146:153], v[162:169], v[60:63]
	v_mfma_f32_16x16x128_f8f6f4 v[56:59], v[154:161], v[162:169], v[56:59]
	v_mfma_f32_16x16x128_f8f6f4 v[44:47], v[146:153], v[180:187], v[44:47]
	v_mfma_f32_16x16x128_f8f6f4 v[40:43], v[154:161], v[180:187], v[40:43]
	v_mfma_f32_16x16x128_f8f6f4 v[28:31], v[146:153], v[188:195], v[28:31]
	v_mfma_f32_16x16x128_f8f6f4 v[24:27], v[154:161], v[188:195], v[24:27]
	v_mfma_f32_16x16x128_f8f6f4 v[136:139], v[146:153], v[196:203], v[4:7]
	v_mfma_f32_16x16x128_f8f6f4 v[140:143], v[154:161], v[196:203], v[0:3]
	s_setprio 0
	s_barrier
	s_add_i32 s70, 0, 0x18000
	s_add_i32 s71, 0, 0x1c000
	s_nop 2
	v_add_u32_e32 v0, s70, v176
	v_add_u32_e32 v12, s71, v176
	ds_read_b128 v[146:149], v0
	ds_read_b128 v[150:153], v0 offset:1024
	ds_read_b128 v[154:157], v0 offset:2048
	ds_read_b128 v[158:161], v0 offset:3072
	ds_read_b128 v[0:3], v12
	ds_read_b128 v[4:7], v12 offset:1024
	ds_read_b128 v[8:11], v12 offset:2048
	ds_read_b128 v[12:15], v12 offset:3072
	s_add_u32 s68, s30, 0x40000
	v_mov_b32_e32 v170, v175
	s_addc_u32 s69, s31, 0
	s_mov_b32 m0, s42
	ds_read_b128 v[162:165], v179 offset:32768
	ds_read_b128 v[166:169], v179 offset:33792
	ds_read_b128 v[180:183], v179 offset:34816
	ds_read_b128 v[184:187], v179 offset:35840
	ds_read_b128 v[188:191], v179 offset:36864
	ds_read_b128 v[192:195], v179 offset:37888
	ds_read_b128 v[196:199], v179 offset:38912
	ds_read_b128 v[200:203], v179 offset:39936
	s_nop 0
	global_load_lds_dwordx4 v170, s[68:69]
	s_add_u32 s68, s30, 0x60000
	v_mov_b32_e32 v170, v175
	s_addc_u32 s69, s31, 0
	s_mov_b32 m0, s43
	s_nop 0
	global_load_lds_dwordx4 v170, s[68:69]
	s_waitcnt vmcnt(8)
	s_waitcnt lgkmcnt(0)
	s_barrier
	s_setprio 3
	s_waitcnt lgkmcnt(0)
	v_mfma_f32_16x16x128_f8f6f4 v[132:135], v[146:153], v[162:169], v[132:135]
	v_mfma_f32_16x16x128_f8f6f4 v[128:131], v[154:161], v[162:169], v[128:131]
	v_mfma_f32_16x16x128_f8f6f4 v[116:119], v[146:153], v[180:187], v[116:119]
	v_mfma_f32_16x16x128_f8f6f4 v[112:115], v[154:161], v[180:187], v[112:115]
	v_mfma_f32_16x16x128_f8f6f4 v[100:103], v[146:153], v[188:195], v[100:103]
	v_mfma_f32_16x16x128_f8f6f4 v[96:99], v[154:161], v[188:195], v[96:99]
	v_mfma_f32_16x16x128_f8f6f4 v[84:87], v[146:153], v[196:203], v[84:87]
	v_mfma_f32_16x16x128_f8f6f4 v[80:83], v[154:161], v[196:203], v[80:83]
	v_mfma_f32_16x16x128_f8f6f4 v[124:127], v[0:7], v[162:169], v[124:127]
	v_mfma_f32_16x16x128_f8f6f4 v[120:123], v[8:15], v[162:169], v[120:123]
	v_mfma_f32_16x16x128_f8f6f4 v[108:111], v[0:7], v[180:187], v[108:111]
	v_mfma_f32_16x16x128_f8f6f4 v[104:107], v[8:15], v[180:187], v[104:107]
	v_mfma_f32_16x16x128_f8f6f4 v[92:95], v[0:7], v[188:195], v[92:95]
	v_mfma_f32_16x16x128_f8f6f4 v[88:91], v[8:15], v[188:195], v[88:91]
	v_mfma_f32_16x16x128_f8f6f4 v[76:79], v[0:7], v[196:203], v[76:79]
	v_mfma_f32_16x16x128_f8f6f4 v[72:75], v[8:15], v[196:203], v[72:75]
	s_setprio 0
	s_barrier
	s_add_u32 s68, s36, 0x80
	s_addc_u32 s69, s37, 0
	v_mov_b32_e32 v170, v174
	s_add_i32 s70, s70, s39
	ds_read_b128 v[162:165], v179 offset:49152
	ds_read_b128 v[166:169], v179 offset:50176
	ds_read_b128 v[180:183], v179 offset:51200
	ds_read_b128 v[184:187], v179 offset:52224
	ds_read_b128 v[188:191], v179 offset:53248
	ds_read_b128 v[192:195], v179 offset:54272
	ds_read_b128 v[196:199], v179 offset:55296
	ds_read_b128 v[200:203], v179 offset:56320
	s_mov_b32 m0, s70
	s_nop 0
	global_load_lds_dwordx4 v170, s[68:69]
	s_add_u32 s68, s36, 0x20080
	v_mov_b32_e32 v170, v174
	s_addc_u32 s69, s37, 0
	s_add_i32 m0, s70, 0x2000
	s_nop 0
	global_load_lds_dwordx4 v170, s[68:69]
	s_add_u32 s68, s36, 0x40080
	v_mov_b32_e32 v170, v174
	s_addc_u32 s69, s37, 0
	s_add_i32 s70, s71, s39
	s_mov_b32 m0, s70
	s_add_u32 s36, s36, 0x60080
	global_load_lds_dwordx4 v170, s[68:69]
	v_mov_b32_e32 v170, v174
	s_addc_u32 s37, s37, 0
	s_add_i32 m0, s70, 0x2000
	s_add_u32 s30, s30, 0x20080
	global_load_lds_dwordx4 v170, s[36:37]
	v_mov_b32_e32 v170, v175
	s_mov_b32 m0, s53
	s_addc_u32 s31, s31, 0
	global_load_lds_dwordx4 v170, s[34:35]
	v_mov_b32_e32 v170, v175
	s_mov_b32 m0, s54
	s_nop 0
	global_load_lds_dwordx4 v170, s[30:31]
	s_waitcnt vmcnt(8)
	s_waitcnt lgkmcnt(0)
	s_barrier
	s_setprio 3
	s_waitcnt lgkmcnt(0)
	v_mfma_f32_16x16x128_f8f6f4 v[68:71], v[146:153], v[162:169], v[68:71]
	v_mfma_f32_16x16x128_f8f6f4 v[64:67], v[154:161], v[162:169], v[64:67]
	v_mfma_f32_16x16x128_f8f6f4 v[52:55], v[146:153], v[180:187], v[52:55]
	v_mfma_f32_16x16x128_f8f6f4 v[48:51], v[154:161], v[180:187], v[48:51]
	v_mfma_f32_16x16x128_f8f6f4 v[36:39], v[146:153], v[188:195], v[36:39]
	v_mfma_f32_16x16x128_f8f6f4 v[32:35], v[154:161], v[188:195], v[32:35]
	v_mfma_f32_16x16x128_f8f6f4 v[20:23], v[146:153], v[196:203], v[20:23]
	v_mfma_f32_16x16x128_f8f6f4 v[16:19], v[154:161], v[196:203], v[16:19]
	v_mfma_f32_16x16x128_f8f6f4 v[60:63], v[0:7], v[162:169], v[60:63]
	v_mfma_f32_16x16x128_f8f6f4 v[56:59], v[8:15], v[162:169], v[56:59]
	v_mfma_f32_16x16x128_f8f6f4 v[44:47], v[0:7], v[180:187], v[44:47]
	v_mfma_f32_16x16x128_f8f6f4 v[40:43], v[8:15], v[180:187], v[40:43]
	v_mfma_f32_16x16x128_f8f6f4 v[28:31], v[0:7], v[188:195], v[28:31]
	v_mfma_f32_16x16x128_f8f6f4 v[24:27], v[8:15], v[188:195], v[24:27]
	v_mfma_f32_16x16x128_f8f6f4 v[4:7], v[0:7], v[196:203], v[136:139]
	v_mfma_f32_16x16x128_f8f6f4 v[0:3], v[8:15], v[196:203], v[140:143]
	s_setprio 0
	s_barrier
	s_add_i32 s65, s65, 2
	s_add_u32 s19, s19, 0x100
	s_addc_u32 s21, s21, 0
	s_add_u32 s28, s28, 0x100
	s_addc_u32 s29, s29, 0
	s_cmp_gt_u32 s65, 13
	s_cbranch_scc0 .LBB0_2137
	s_and_b64 vcc, exec, s[12:13]
	s_cbranch_vccz .LBB0_2140
	s_barrier

.LBB0_2446:
	ds_read_b128 v[144:147], v137
	ds_read_b128 v[148:151], v137 offset:1024
	ds_read_b128 v[152:155], v137 offset:2048
	ds_read_b128 v[156:159], v137 offset:3072
	ds_read_b128 v[160:163], v138
	ds_read_b128 v[164:167], v138 offset:1024
	ds_read_b128 v[168:171], v138 offset:2048
	ds_read_b128 v[172:175], v138 offset:3072
	s_cmp_eq_u32 s60, 4
	s_cselect_b64 vcc, -1, 0
	s_and_b64 s[22:23], vcc, exec
	s_cselect_b32 s26, s8, s58
	s_cselect_b32 s27, s9, s59
	s_cselect_b32 s24, s20, s14
	s_cselect_b32 s25, s21, s57
	s_add_u32 s22, s26, 0x80
	s_addc_u32 s23, s27, 0
	s_add_u32 s62, s58, 0xffffff80
	s_addc_u32 s63, s59, -1
	v_mov_b32_e32 v132, v130
	s_mov_b32 m0, s50
	ds_read_b128 v[176:179], v139
	ds_read_b128 v[180:183], v139 offset:1024
	ds_read_b128 v[184:187], v139 offset:2048
	ds_read_b128 v[188:191], v139 offset:3072
	ds_read_b128 v[192:195], v139 offset:4096
	ds_read_b128 v[196:199], v139 offset:5120
	ds_read_b128 v[200:203], v139 offset:6144
	ds_read_b128 v[204:207], v139 offset:7168
	s_mov_b64 s[64:65], s[62:63]
	s_nop 0
	global_load_lds_dwordx4 v132, s[64:65]
	v_mov_b32_e32 v132, v131
	s_mov_b32 m0, s51
	s_nop 0
	global_load_lds_dwordx4 v132, s[62:63]
	s_waitcnt vmcnt(8)
	s_waitcnt lgkmcnt(0)
	s_barrier
	s_setprio 3
	s_waitcnt lgkmcnt(0)
	v_mfma_f32_16x16x128_f8f6f4 v[124:127], v[144:151], v[176:183], v[124:127]
	v_mfma_f32_16x16x128_f8f6f4 v[116:119], v[152:159], v[176:183], v[116:119]
	v_mfma_f32_16x16x128_f8f6f4 v[108:111], v[144:151], v[184:191], v[108:111]
	v_mfma_f32_16x16x128_f8f6f4 v[100:103], v[152:159], v[184:191], v[100:103]
	v_mfma_f32_16x16x128_f8f6f4 v[92:95], v[144:151], v[192:199], v[92:95]
	v_mfma_f32_16x16x128_f8f6f4 v[84:87], v[152:159], v[192:199], v[84:87]
	v_mfma_f32_16x16x128_f8f6f4 v[76:79], v[144:151], v[200:207], v[76:79]
	v_mfma_f32_16x16x128_f8f6f4 v[68:71], v[152:159], v[200:207], v[68:71]
	v_mfma_f32_16x16x128_f8f6f4 v[120:123], v[160:167], v[176:183], v[120:123]
	v_mfma_f32_16x16x128_f8f6f4 v[112:115], v[168:175], v[176:183], v[112:115]
	v_mfma_f32_16x16x128_f8f6f4 v[104:107], v[160:167], v[184:191], v[104:107]
	v_mfma_f32_16x16x128_f8f6f4 v[96:99], v[168:175], v[184:191], v[96:99]
	v_mfma_f32_16x16x128_f8f6f4 v[88:91], v[160:167], v[192:199], v[88:91]
	v_mfma_f32_16x16x128_f8f6f4 v[80:83], v[168:175], v[192:199], v[80:83]
	v_mfma_f32_16x16x128_f8f6f4 v[72:75], v[160:167], v[200:207], v[72:75]
	v_mfma_f32_16x16x128_f8f6f4 v[64:67], v[168:175], v[200:207], v[64:67]
	s_setprio 0
	s_barrier
	v_mov_b32_e32 v132, v134
	s_mov_b64 s[62:63], s[24:25]
	s_mov_b32 m0, s52
	ds_read_b128 v[176:179], v139 offset:16384
	ds_read_b128 v[180:183], v139 offset:17408
	ds_read_b128 v[184:187], v139 offset:18432
	ds_read_b128 v[188:191], v139 offset:19456
	ds_read_b128 v[192:195], v139 offset:20480
	ds_read_b128 v[196:199], v139 offset:21504
	ds_read_b128 v[200:203], v139 offset:22528
	ds_read_b128 v[204:207], v139 offset:23552
	s_nop 0
	global_load_lds_dwordx4 v132, s[62:63]
	s_add_u32 s62, s24, 0x10000
	v_mov_b32_e32 v132, v134
	s_addc_u32 s63, s25, 0
	s_add_i32 m0, s52, 0x2000
	s_nop 0
	global_load_lds_dwordx4 v132, s[62:63]
	s_add_u32 s62, s24, 0x20000
	v_mov_b32_e32 v132, v134
	s_addc_u32 s63, s25, 0
	s_add_i32 s61, s45, s34
	s_mov_b32 m0, s61
	s_nop 0
	global_load_lds_dwordx4 v132, s[62:63]
	v_mov_b32_e32 v132, v134
	s_add_u32 s62, s24, 0x30000
	s_addc_u32 s63, s25, 0
	s_add_i32 m0, s61, 0x2000
	s_nop 0
	global_load_lds_dwordx4 v132, s[62:63]
	v_cndmask_b32_e32 v132, v128, v141, vcc
	v_lshlrev_b32_e32 v133, 10, v132
	v_and_or_b32 v133, v133, s36, v135
	v_mov_b32_e32 v143, v133
	s_mov_b64 s[62:63], s[26:27]
	s_mov_b32 m0, s35
	s_nop 0
	global_load_lds_dwordx4 v143, s[62:63]
	v_cndmask_b32_e32 v143, v129, v142, vcc
	v_lshlrev_b32_e32 v208, 10, v143
	v_and_or_b32 v208, v208, s36, v135
	v_mov_b32_e32 v209, v208
	s_mov_b64 s[62:63], s[26:27]
	s_mov_b32 m0, s37
	s_nop 0
	global_load_lds_dwordx4 v209, s[62:63]
	s_waitcnt vmcnt(8)
	s_waitcnt lgkmcnt(0)
	s_barrier
	s_setprio 3
	s_waitcnt lgkmcnt(0)
	v_mfma_f32_16x16x128_f8f6f4 v[60:63], v[144:151], v[176:183], v[60:63]
	v_mfma_f32_16x16x128_f8f6f4 v[52:55], v[152:159], v[176:183], v[52:55]
	v_mfma_f32_16x16x128_f8f6f4 v[44:47], v[144:151], v[184:191], v[44:47]
	v_mfma_f32_16x16x128_f8f6f4 v[36:39], v[152:159], v[184:191], v[36:39]
	v_mfma_f32_16x16x128_f8f6f4 v[28:31], v[144:151], v[192:199], v[28:31]
	v_mfma_f32_16x16x128_f8f6f4 v[20:23], v[152:159], v[192:199], v[20:23]
	v_mfma_f32_16x16x128_f8f6f4 v[12:15], v[144:151], v[200:207], v[12:15]
	v_mfma_f32_16x16x128_f8f6f4 v[4:7], v[152:159], v[200:207], v[4:7]
	v_mfma_f32_16x16x128_f8f6f4 v[56:59], v[160:167], v[176:183], v[56:59]
	v_mfma_f32_16x16x128_f8f6f4 v[48:51], v[168:175], v[176:183], v[48:51]
	v_mfma_f32_16x16x128_f8f6f4 v[40:43], v[160:167], v[184:191], v[40:43]
	v_mfma_f32_16x16x128_f8f6f4 v[32:35], v[168:175], v[184:191], v[32:35]
	v_mfma_f32_16x16x128_f8f6f4 v[24:27], v[160:167], v[192:199], v[24:27]
	v_mfma_f32_16x16x128_f8f6f4 v[16:19], v[168:175], v[192:199], v[16:19]
	v_mfma_f32_16x16x128_f8f6f4 v[8:11], v[160:167], v[200:207], v[8:11]
	v_mfma_f32_16x16x128_f8f6f4 v[0:3], v[168:175], v[200:207], v[0:3]
	s_setprio 0
	s_barrier
	s_add_i32 s61, 0, 0x18000
	s_add_i32 s64, 0, 0x1c000
	v_add_u32_e32 v156, s61, v136
	v_add_u32_e32 v172, s64, v136
	ds_read_b128 v[144:147], v156
	ds_read_b128 v[148:151], v156 offset:1024
	ds_read_b128 v[152:155], v156 offset:2048
	ds_read_b128 v[156:159], v156 offset:3072
	ds_read_b128 v[160:163], v172
	ds_read_b128 v[164:167], v172 offset:1024
	ds_read_b128 v[168:171], v172 offset:2048
	ds_read_b128 v[172:175], v172 offset:3072
	v_bfe_u32 v132, v132, 16, 16
	v_lshl_or_b32 v132, v132, 10, v135
	s_mov_b32 m0, s38
	ds_read_b128 v[176:179], v139 offset:32768
	ds_read_b128 v[180:183], v139 offset:33792
	ds_read_b128 v[184:187], v139 offset:34816
	ds_read_b128 v[188:191], v139 offset:35840
	ds_read_b128 v[192:195], v139 offset:36864
	ds_read_b128 v[196:199], v139 offset:37888
	ds_read_b128 v[200:203], v139 offset:38912
	ds_read_b128 v[204:207], v139 offset:39936
	s_mov_b64 s[62:63], s[26:27]
	s_nop 0
	global_load_lds_dwordx4 v132, s[62:63]
	v_bfe_u32 v132, v143, 16, 16
	v_lshl_or_b32 v132, v132, 10, v135
	s_mov_b32 m0, s39
	s_nop 0
	global_load_lds_dwordx4 v132, s[26:27]
	s_waitcnt vmcnt(8)
	s_waitcnt lgkmcnt(0)
	s_barrier
	s_setprio 3
	s_waitcnt lgkmcnt(0)
	v_mfma_f32_16x16x128_f8f6f4 v[124:127], v[144:151], v[176:183], v[124:127]
	v_mfma_f32_16x16x128_f8f6f4 v[116:119], v[152:159], v[176:183], v[116:119]
	v_mfma_f32_16x16x128_f8f6f4 v[108:111], v[144:151], v[184:191], v[108:111]
	v_mfma_f32_16x16x128_f8f6f4 v[100:103], v[152:159], v[184:191], v[100:103]
	v_mfma_f32_16x16x128_f8f6f4 v[92:95], v[144:151], v[192:199], v[92:95]
	v_mfma_f32_16x16x128_f8f6f4 v[84:87], v[152:159], v[192:199], v[84:87]
	v_mfma_f32_16x16x128_f8f6f4 v[76:79], v[144:151], v[200:207], v[76:79]
	v_mfma_f32_16x16x128_f8f6f4 v[68:71], v[152:159], v[200:207], v[68:71]
	v_mfma_f32_16x16x128_f8f6f4 v[120:123], v[160:167], v[176:183], v[120:123]
	v_mfma_f32_16x16x128_f8f6f4 v[112:115], v[168:175], v[176:183], v[112:115]
	v_mfma_f32_16x16x128_f8f6f4 v[104:107], v[160:167], v[184:191], v[104:107]
	v_mfma_f32_16x16x128_f8f6f4 v[96:99], v[168:175], v[184:191], v[96:99]
	v_mfma_f32_16x16x128_f8f6f4 v[88:91], v[160:167], v[192:199], v[88:91]
	v_mfma_f32_16x16x128_f8f6f4 v[80:83], v[168:175], v[192:199], v[80:83]
	v_mfma_f32_16x16x128_f8f6f4 v[72:75], v[160:167], v[200:207], v[72:75]
	v_mfma_f32_16x16x128_f8f6f4 v[64:67], v[168:175], v[200:207], v[64:67]
	s_setprio 0
	s_barrier
	s_add_u32 s26, s24, 0x80
	s_addc_u32 s27, s25, 0
	v_mov_b32_e32 v132, v134
	s_add_i32 s61, s61, s34
	ds_read_b128 v[176:179], v139 offset:49152
	ds_read_b128 v[180:183], v139 offset:50176
	ds_read_b128 v[184:187], v139 offset:51200
	ds_read_b128 v[188:191], v139 offset:52224
	ds_read_b128 v[192:195], v139 offset:53248
	ds_read_b128 v[196:199], v139 offset:54272
	ds_read_b128 v[200:203], v139 offset:55296
	ds_read_b128 v[204:207], v139 offset:56320
	s_mov_b32 m0, s61
	s_nop 0
	global_load_lds_dwordx4 v132, s[26:27]
	s_add_u32 s26, s24, 0x10080
	v_mov_b32_e32 v132, v134
	s_addc_u32 s27, s25, 0
	s_add_i32 m0, s61, 0x2000
	s_nop 0
	global_load_lds_dwordx4 v132, s[26:27]
	s_add_u32 s26, s24, 0x20080
	v_mov_b32_e32 v132, v134
	s_addc_u32 s27, s25, 0
	s_add_i32 s61, s64, s34
	s_mov_b32 m0, s61
	s_add_u32 s24, s24, 0x30080
	s_addc_u32 s25, s25, 0
	global_load_lds_dwordx4 v132, s[26:27]
	v_mov_b32_e32 v132, v134
	s_add_i32 m0, s61, 0x2000
	s_nop 0
	global_load_lds_dwordx4 v132, s[24:25]
	s_mov_b64 s[24:25], s[22:23]
	s_mov_b32 m0, s42
	s_nop 0
	global_load_lds_dwordx4 v133, s[24:25]
	s_mov_b32 m0, s43
	s_nop 0
	global_load_lds_dwordx4 v208, s[22:23]
	s_waitcnt vmcnt(8)
	s_waitcnt lgkmcnt(0)
	s_barrier
	s_setprio 3
	s_waitcnt lgkmcnt(0)
	v_mfma_f32_16x16x128_f8f6f4 v[60:63], v[144:151], v[176:183], v[60:63]
	v_mfma_f32_16x16x128_f8f6f4 v[52:55], v[152:159], v[176:183], v[52:55]
	v_mfma_f32_16x16x128_f8f6f4 v[44:47], v[144:151], v[184:191], v[44:47]
	v_mfma_f32_16x16x128_f8f6f4 v[36:39], v[152:159], v[184:191], v[36:39]
	v_mfma_f32_16x16x128_f8f6f4 v[28:31], v[144:151], v[192:199], v[28:31]
	v_mfma_f32_16x16x128_f8f6f4 v[20:23], v[152:159], v[192:199], v[20:23]
	v_mfma_f32_16x16x128_f8f6f4 v[12:15], v[144:151], v[200:207], v[12:15]
	v_mfma_f32_16x16x128_f8f6f4 v[4:7], v[152:159], v[200:207], v[4:7]
	v_mfma_f32_16x16x128_f8f6f4 v[56:59], v[160:167], v[176:183], v[56:59]
	v_mfma_f32_16x16x128_f8f6f4 v[48:51], v[168:175], v[176:183], v[48:51]
	v_mfma_f32_16x16x128_f8f6f4 v[40:43], v[160:167], v[184:191], v[40:43]
	v_mfma_f32_16x16x128_f8f6f4 v[32:35], v[168:175], v[184:191], v[32:35]
	v_mfma_f32_16x16x128_f8f6f4 v[24:27], v[160:167], v[192:199], v[24:27]
	v_mfma_f32_16x16x128_f8f6f4 v[16:19], v[168:175], v[192:199], v[16:19]
	v_mfma_f32_16x16x128_f8f6f4 v[8:11], v[160:167], v[200:207], v[8:11]
	v_mfma_f32_16x16x128_f8f6f4 v[0:3], v[168:175], v[200:207], v[0:3]
	s_setprio 0
	s_barrier
	s_add_i32 s60, s60, 2
	s_add_u32 s14, s14, 0x100
	s_addc_u32 s57, s57, 0
	s_add_u32 s58, s58, 0x100
	s_addc_u32 s59, s59, 0
	s_cmp_gt_u32 s60, 5
	s_cbranch_scc0 .LBB0_2446
	s_and_b64 vcc, exec, s[18:19]
	s_cbranch_vccz .LBB0_2449
	s_barrier

.LBB0_2608:
	ds_read_b128 v[72:75], v67
	ds_read_b128 v[76:79], v67 offset:1024
	ds_read_b128 v[80:83], v67 offset:2048
	ds_read_b128 v[84:87], v67 offset:3072
	ds_read_b128 v[88:91], v68
	ds_read_b128 v[92:95], v68 offset:1024
	ds_read_b128 v[96:99], v68 offset:2048
	ds_read_b128 v[100:103], v68 offset:3072
	s_cmp_eq_u32 s36, 4
	s_cselect_b32 s16, s8, s34
	s_cselect_b32 s17, s9, s35
	s_cselect_b32 s14, s0, s30
	s_cselect_b32 s15, s1, s31
	s_add_u32 s4, s16, 0x80
	s_addc_u32 s5, s17, 0
	ds_read_b128 v[104:107], v69
	ds_read_b128 v[108:111], v69 offset:1024
	ds_read_b128 v[112:115], v69 offset:2048
	ds_read_b128 v[116:119], v69 offset:3072
	ds_read_b128 v[120:123], v69 offset:4096
	ds_read_b128 v[124:127], v69 offset:5120
	ds_read_b128 v[128:131], v69 offset:6144
	ds_read_b128 v[132:135], v69 offset:7168
	s_waitcnt vmcnt(6)
	s_waitcnt lgkmcnt(0)
	s_barrier
	s_setprio 3
	s_waitcnt lgkmcnt(0)
	v_mfma_f32_16x16x128_f8f6f4 v[60:63], v[72:79], v[104:111], v[60:63]
	v_mfma_f32_16x16x128_f8f6f4 v[52:55], v[80:87], v[104:111], v[52:55]
	v_mfma_f32_16x16x128_f8f6f4 v[44:47], v[72:79], v[112:119], v[44:47]
	v_mfma_f32_16x16x128_f8f6f4 v[36:39], v[80:87], v[112:119], v[36:39]
	v_mfma_f32_16x16x128_f8f6f4 v[28:31], v[72:79], v[120:127], v[28:31]
	v_mfma_f32_16x16x128_f8f6f4 v[20:23], v[80:87], v[120:127], v[20:23]
	v_mfma_f32_16x16x128_f8f6f4 v[12:15], v[72:79], v[128:135], v[12:15]
	v_mfma_f32_16x16x128_f8f6f4 v[136:139], v[80:87], v[128:135], v[4:7]
	v_mfma_f32_16x16x128_f8f6f4 v[56:59], v[88:95], v[104:111], v[56:59]
	v_mfma_f32_16x16x128_f8f6f4 v[48:51], v[96:103], v[104:111], v[48:51]
	v_mfma_f32_16x16x128_f8f6f4 v[40:43], v[88:95], v[112:119], v[40:43]
	v_mfma_f32_16x16x128_f8f6f4 v[32:35], v[96:103], v[112:119], v[32:35]
	v_mfma_f32_16x16x128_f8f6f4 v[24:27], v[88:95], v[120:127], v[24:27]
	v_mfma_f32_16x16x128_f8f6f4 v[16:19], v[96:103], v[120:127], v[16:19]
	v_mfma_f32_16x16x128_f8f6f4 v[8:11], v[88:95], v[128:135], v[8:11]
	v_mfma_f32_16x16x128_f8f6f4 v[128:131], v[96:103], v[128:135], v[0:3]
	s_setprio 0
	s_barrier
	s_nop 4
	v_mov_b32_e32 v0, v64
	s_mov_b64 s[50:51], s[14:15]
	s_mov_b32 m0, s37
	s_nop 0
	global_load_lds_dwordx4 v0, s[50:51]
	s_add_u32 s50, s14, 0x10000
	v_mov_b32_e32 v0, v64
	s_addc_u32 s51, s15, 0
	s_mov_b32 m0, s38
	s_nop 0
	global_load_lds_dwordx4 v0, s[50:51]
	s_add_u32 s50, s14, 0x20000
	v_mov_b32_e32 v0, v64
	s_addc_u32 s51, s15, 0
	s_mov_b32 m0, s39
	s_nop 0
	global_load_lds_dwordx4 v0, s[50:51]
	v_mov_b32_e32 v0, v64
	s_add_u32 s50, s14, 0x30000
	s_addc_u32 s51, s15, 0
	s_mov_b32 m0, s40
	s_nop 0
	global_load_lds_dwordx4 v0, s[50:51]
	v_mov_b32_e32 v0, v65
	s_mov_b64 s[50:51], s[16:17]
	s_mov_b32 m0, s23
	s_nop 0
	global_load_lds_dwordx4 v0, s[50:51]
	v_mov_b32_e32 v0, v66
	s_mov_b32 m0, s25
	s_nop 0
	global_load_lds_dwordx4 v0, s[16:17]
	s_waitcnt vmcnt(6)
	s_waitcnt lgkmcnt(0)
	s_barrier
	s_barrier
	ds_read_b128 v[0:3], v70
	ds_read_b128 v[4:7], v70 offset:1024
	ds_read_b128 v[72:75], v70 offset:2048
	ds_read_b128 v[76:79], v70 offset:3072
	ds_read_b128 v[80:83], v71
	ds_read_b128 v[84:87], v71 offset:1024
	ds_read_b128 v[88:91], v71 offset:2048
	ds_read_b128 v[92:95], v71 offset:3072
	ds_read_b128 v[96:99], v69 offset:32768
	ds_read_b128 v[100:103], v69 offset:33792
	ds_read_b128 v[104:107], v69 offset:34816
	ds_read_b128 v[108:111], v69 offset:35840
	ds_read_b128 v[112:115], v69 offset:36864
	ds_read_b128 v[116:119], v69 offset:37888
	ds_read_b128 v[120:123], v69 offset:38912
	ds_read_b128 v[124:127], v69 offset:39936
	s_waitcnt vmcnt(6)
	s_waitcnt lgkmcnt(0)
	s_barrier
	s_setprio 3
	s_waitcnt lgkmcnt(0)
	v_mfma_f32_16x16x128_f8f6f4 v[60:63], v[0:7], v[96:103], v[60:63]
	v_mfma_f32_16x16x128_f8f6f4 v[52:55], v[72:79], v[96:103], v[52:55]
	v_mfma_f32_16x16x128_f8f6f4 v[44:47], v[0:7], v[104:111], v[44:47]
	v_mfma_f32_16x16x128_f8f6f4 v[36:39], v[72:79], v[104:111], v[36:39]
	v_mfma_f32_16x16x128_f8f6f4 v[28:31], v[0:7], v[112:119], v[28:31]
	v_mfma_f32_16x16x128_f8f6f4 v[20:23], v[72:79], v[112:119], v[20:23]
	v_mfma_f32_16x16x128_f8f6f4 v[12:15], v[0:7], v[120:127], v[12:15]
	v_mfma_f32_16x16x128_f8f6f4 v[4:7], v[72:79], v[120:127], v[136:139]
	v_mfma_f32_16x16x128_f8f6f4 v[56:59], v[80:87], v[96:103], v[56:59]
	s_add_u32 s16, s14, 0x80
	s_addc_u32 s17, s15, 0
	v_mfma_f32_16x16x128_f8f6f4 v[48:51], v[88:95], v[96:103], v[48:51]
	v_mfma_f32_16x16x128_f8f6f4 v[40:43], v[80:87], v[104:111], v[40:43]
	v_mfma_f32_16x16x128_f8f6f4 v[32:35], v[88:95], v[104:111], v[32:35]
	v_mfma_f32_16x16x128_f8f6f4 v[24:27], v[80:87], v[112:119], v[24:27]
	v_mfma_f32_16x16x128_f8f6f4 v[16:19], v[88:95], v[112:119], v[16:19]
	v_mfma_f32_16x16x128_f8f6f4 v[8:11], v[80:87], v[120:127], v[8:11]
	v_mfma_f32_16x16x128_f8f6f4 v[0:3], v[88:95], v[120:127], v[128:131]
	s_setprio 0
	s_barrier
	v_mov_b32_e32 v72, v64
	s_mov_b32 m0, s41
	s_nop 0
	global_load_lds_dwordx4 v72, s[16:17]
	s_add_u32 s16, s14, 0x10080
	v_mov_b32_e32 v72, v64
	s_addc_u32 s17, s15, 0
	s_mov_b32 m0, s42
	s_nop 0
	global_load_lds_dwordx4 v72, s[16:17]
	v_mov_b32_e32 v72, v64
	s_add_u32 s16, s14, 0x20080
	s_addc_u32 s17, s15, 0
	s_mov_b32 m0, s43
	s_add_u32 s14, s14, 0x30080
	global_load_lds_dwordx4 v72, s[16:17]
	v_mov_b32_e32 v72, v64
	s_addc_u32 s15, s15, 0
	s_mov_b32 m0, s44
	s_nop 0
	global_load_lds_dwordx4 v72, s[14:15]
	v_mov_b32_e32 v72, v65
	s_mov_b64 s[14:15], s[4:5]
	s_mov_b32 m0, s26
	s_nop 0
	global_load_lds_dwordx4 v72, s[14:15]
	v_mov_b32_e32 v72, v66
	s_mov_b32 m0, s27
	s_nop 0
	global_load_lds_dwordx4 v72, s[4:5]
	s_waitcnt vmcnt(6)
	s_waitcnt lgkmcnt(0)
	s_barrier
	s_barrier
	s_add_i32 s36, s36, 2
	s_add_u32 s30, s30, 0x100
	s_addc_u32 s31, s31, 0
	s_add_u32 s34, s34, 0x100
	s_addc_u32 s35, s35, 0
	s_cmp_gt_u32 s36, 5
	s_cbranch_scc0 .LBB0_2608
	s_cmpk_lt_u32 s22, 0x100
	s_cbranch_scc0 .LBB0_2611
	s_barrier

.LBB0_2724:
	ds_read_b128 v[56:59], v197
	ds_read_b128 v[60:63], v197 offset:1024
	ds_read_b128 v[80:83], v197 offset:2048
	ds_read_b128 v[84:87], v197 offset:3072
	ds_read_b128 v[0:3], v198
	ds_read_b128 v[4:7], v198 offset:1024
	ds_read_b128 v[8:11], v198 offset:2048
	ds_read_b128 v[12:15], v198 offset:3072
	s_add_u32 s42, s34, 0x80
	s_addc_u32 s43, s35, 0
	s_add_u32 s44, s14, 0x80
	s_addc_u32 s45, s15, 0
	s_add_u32 s64, s40, 0x8080
	v_mov_b32_e32 v16, v195
	s_addc_u32 s65, s41, 0
	s_add_i32 m0, s50, 0xc000
	ds_read_b128 v[64:67], v199
	ds_read_b128 v[68:71], v199 offset:1024
	ds_read_b128 v[72:75], v199 offset:2048
	ds_read_b128 v[76:79], v199 offset:3072
	ds_read_b128 v[88:91], v199 offset:4096
	ds_read_b128 v[92:95], v199 offset:5120
	ds_read_b128 v[96:99], v199 offset:6144
	ds_read_b128 v[100:103], v199 offset:7168
	s_add_u32 s40, s40, 0xc080
	s_addc_u32 s41, s41, 0
	global_load_lds_dwordx4 v16, s[64:65] sc1
	v_mov_b32_e32 v16, v195
	s_add_i32 m0, s50, 0xe000
	s_nop 0
	global_load_lds_dwordx4 v16, s[40:41] sc1
	s_waitcnt vmcnt(8)
	s_waitcnt lgkmcnt(0)
	s_barrier
	s_setprio 3
	s_waitcnt lgkmcnt(0)
	v_mfma_f32_16x16x128_f8f6f4 v[16:19], v[56:63], v[64:71], 0
	v_mfma_f32_16x16x128_f8f6f4 v[20:23], v[80:87], v[64:71], 0
	v_mfma_f32_16x16x128_f8f6f4 v[24:27], v[56:63], v[72:79], 0
	v_mfma_f32_16x16x128_f8f6f4 v[28:31], v[80:87], v[72:79], 0
	v_mfma_f32_16x16x128_f8f6f4 v[32:35], v[56:63], v[88:95], 0
	v_mfma_f32_16x16x128_f8f6f4 v[36:39], v[80:87], v[88:95], 0
	v_mfma_f32_16x16x128_f8f6f4 v[40:43], v[56:63], v[96:103], 0
	v_mfma_f32_16x16x128_f8f6f4 v[44:47], v[80:87], v[96:103], 0
	v_mfma_f32_16x16x128_f8f6f4 v[48:51], v[0:7], v[64:71], 0
	v_mfma_f32_16x16x128_f8f6f4 v[52:55], v[8:15], v[64:71], 0
	v_mfma_f32_16x16x128_f8f6f4 v[64:67], v[0:7], v[72:79], 0
	v_mfma_f32_16x16x128_f8f6f4 v[68:71], v[8:15], v[72:79], 0
	v_mfma_f32_16x16x128_f8f6f4 v[72:75], v[0:7], v[88:95], 0
	v_mfma_f32_16x16x128_f8f6f4 v[76:79], v[8:15], v[88:95], 0
	v_mfma_f32_16x16x128_f8f6f4 v[128:131], v[0:7], v[96:103], 0
	v_mfma_f32_16x16x128_f8f6f4 v[132:135], v[8:15], v[96:103], 0
	s_setprio 0
	s_barrier
	v_mov_b32_e32 v120, v194
	s_mov_b64 s[40:41], s[14:15]
	s_add_i32 s19, s61, s27
	ds_read_b128 v[88:91], v199 offset:16384
	ds_read_b128 v[92:95], v199 offset:17408
	ds_read_b128 v[96:99], v199 offset:18432
	ds_read_b128 v[100:103], v199 offset:19456
	ds_read_b128 v[104:107], v199 offset:20480
	ds_read_b128 v[108:111], v199 offset:21504
	ds_read_b128 v[112:115], v199 offset:22528
	ds_read_b128 v[116:119], v199 offset:23552
	s_mov_b32 m0, s19
	s_nop 0
	global_load_lds_dwordx4 v120, s[40:41]
	s_add_u32 s40, s14, 0x4000
	v_mov_b32_e32 v120, v194
	s_addc_u32 s41, s15, 0
	s_add_i32 m0, s19, 0x2000
	s_nop 0
	global_load_lds_dwordx4 v120, s[40:41]
	s_add_u32 s40, s14, 0x8000
	v_mov_b32_e32 v120, v194
	s_addc_u32 s41, s15, 0
	s_add_i32 s19, s62, s27
	s_mov_b32 m0, s19
	s_nop 0
	global_load_lds_dwordx4 v120, s[40:41]
	s_add_u32 s40, s14, 0xc000
	v_mov_b32_e32 v120, v194
	s_addc_u32 s41, s15, 0
	s_add_i32 m0, s19, 0x2000
	s_nop 0
	global_load_lds_dwordx4 v120, s[40:41]
	v_mov_b32_e32 v120, v195
	s_mov_b64 s[40:41], s[34:35]
	s_mov_b32 m0, s50
	s_nop 0
	global_load_lds_dwordx4 v120, s[40:41] sc1
	s_add_u32 s40, s34, 0x4000
	v_mov_b32_e32 v120, v195
	s_addc_u32 s41, s35, 0
	s_mov_b32 m0, s51
	s_nop 0
	global_load_lds_dwordx4 v120, s[40:41] sc1
	s_waitcnt vmcnt(8)
	s_waitcnt lgkmcnt(0)
	s_barrier
	s_setprio 3
	s_waitcnt lgkmcnt(0)
	v_mfma_f32_16x16x128_f8f6f4 v[136:139], v[56:63], v[88:95], 0
	v_mfma_f32_16x16x128_f8f6f4 v[140:143], v[80:87], v[88:95], 0
	v_mfma_f32_16x16x128_f8f6f4 v[144:147], v[56:63], v[96:103], 0
	v_mfma_f32_16x16x128_f8f6f4 v[148:151], v[80:87], v[96:103], 0
	v_mfma_f32_16x16x128_f8f6f4 v[152:155], v[56:63], v[104:111], 0
	v_mfma_f32_16x16x128_f8f6f4 v[156:159], v[80:87], v[104:111], 0
	v_mfma_f32_16x16x128_f8f6f4 v[160:163], v[56:63], v[112:119], 0
	v_mfma_f32_16x16x128_f8f6f4 v[164:167], v[80:87], v[112:119], 0
	v_mfma_f32_16x16x128_f8f6f4 v[168:171], v[0:7], v[88:95], 0
	v_mfma_f32_16x16x128_f8f6f4 v[176:179], v[0:7], v[96:103], 0
	v_mfma_f32_16x16x128_f8f6f4 v[184:187], v[0:7], v[104:111], 0
	v_mfma_f32_16x16x128_f8f6f4 v[0:3], v[0:7], v[112:119], 0
	v_mfma_f32_16x16x128_f8f6f4 v[4:7], v[8:15], v[112:119], 0
	v_mfma_f32_16x16x128_f8f6f4 v[172:175], v[8:15], v[88:95], 0
	v_mfma_f32_16x16x128_f8f6f4 v[180:183], v[8:15], v[96:103], 0
	v_mfma_f32_16x16x128_f8f6f4 v[188:191], v[8:15], v[104:111], 0
	s_setprio 0
	s_barrier
	s_add_i32 s19, 0, 0x18000
	v_add_u32_e32 v56, s19, v196
	s_add_i32 s29, 0, 0x1c000
	ds_read_b128 v[8:11], v56
	ds_read_b128 v[12:15], v56 offset:1024
	ds_read_b128 v[200:203], v56 offset:2048
	ds_read_b128 v[204:207], v56 offset:3072
	v_add_u32_e32 v56, s29, v196
	ds_read_b128 v[208:211], v56
	ds_read_b128 v[212:215], v56 offset:1024
	ds_read_b128 v[216:219], v56 offset:2048
	ds_read_b128 v[220:223], v56 offset:3072
	s_add_u32 s40, s34, 0x8000
	v_mov_b32_e32 v56, v195
	s_addc_u32 s41, s35, 0
	s_mov_b32 m0, s52
	ds_read_b128 v[88:91], v199 offset:32768
	ds_read_b128 v[92:95], v199 offset:33792
	ds_read_b128 v[224:227], v199 offset:34816
	ds_read_b128 v[228:231], v199 offset:35840
	ds_read_b128 v[232:235], v199 offset:36864
	ds_read_b128 v[236:239], v199 offset:37888
	ds_read_b128 v[240:243], v199 offset:38912
	ds_read_b128 v[244:247], v199 offset:39936
	s_nop 0
	global_load_lds_dwordx4 v56, s[40:41] sc1
	s_add_u32 s40, s34, 0xc000
	v_mov_b32_e32 v56, v195
	s_addc_u32 s41, s35, 0
	s_mov_b32 m0, s53
	s_nop 0
	global_load_lds_dwordx4 v56, s[40:41] sc1
	s_waitcnt vmcnt(8)
	s_waitcnt lgkmcnt(0)
	s_barrier
	s_setprio 3
	s_waitcnt lgkmcnt(0)
	v_mfma_f32_16x16x128_f8f6f4 v[112:115], v[8:15], v[88:95], v[16:19]
	v_mfma_f32_16x16x128_f8f6f4 v[116:119], v[200:207], v[88:95], v[20:23]
	v_mfma_f32_16x16x128_f8f6f4 v[96:99], v[8:15], v[224:231], v[24:27]
	v_mfma_f32_16x16x128_f8f6f4 v[100:103], v[200:207], v[224:231], v[28:31]
	v_mfma_f32_16x16x128_f8f6f4 v[80:83], v[8:15], v[232:239], v[32:35]
	v_mfma_f32_16x16x128_f8f6f4 v[84:87], v[200:207], v[232:239], v[36:39]
	v_mfma_f32_16x16x128_f8f6f4 v[56:59], v[8:15], v[240:247], v[40:43]
	v_mfma_f32_16x16x128_f8f6f4 v[60:63], v[200:207], v[240:247], v[44:47]
	v_mfma_f32_16x16x128_f8f6f4 v[120:123], v[208:215], v[88:95], v[48:51]
	v_mfma_f32_16x16x128_f8f6f4 v[124:127], v[216:223], v[88:95], v[52:55]
	v_mfma_f32_16x16x128_f8f6f4 v[104:107], v[208:215], v[224:231], v[64:67]
	v_mfma_f32_16x16x128_f8f6f4 v[108:111], v[216:223], v[224:231], v[68:71]
	v_mfma_f32_16x16x128_f8f6f4 v[88:91], v[208:215], v[232:239], v[72:75]
	v_mfma_f32_16x16x128_f8f6f4 v[92:95], v[216:223], v[232:239], v[76:79]
	v_mfma_f32_16x16x128_f8f6f4 v[64:67], v[208:215], v[240:247], v[128:131]
	v_mfma_f32_16x16x128_f8f6f4 v[68:71], v[216:223], v[240:247], v[132:135]
	s_setprio 0
	s_barrier
	v_mov_b32_e32 v24, v194
	s_add_i32 s19, s19, s27
	ds_read_b128 v[16:19], v199 offset:49152
	ds_read_b128 v[20:23], v199 offset:50176
	ds_read_b128 v[128:131], v199 offset:51200
	ds_read_b128 v[132:135], v199 offset:52224
	ds_read_b128 v[224:227], v199 offset:53248
	ds_read_b128 v[228:231], v199 offset:54272
	ds_read_b128 v[232:235], v199 offset:55296
	ds_read_b128 v[236:239], v199 offset:56320
	s_mov_b32 m0, s19
	s_add_u32 s40, s14, 0x4080
	s_addc_u32 s41, s15, 0
	global_load_lds_dwordx4 v24, s[44:45]
	v_mov_b32_e32 v24, v194
	s_add_i32 m0, s19, 0x2000
	s_nop 0
	global_load_lds_dwordx4 v24, s[40:41]
	s_add_u32 s40, s14, 0x8080
	v_mov_b32_e32 v24, v194
	s_addc_u32 s41, s15, 0
	s_add_i32 s19, s29, s27
	s_mov_b32 m0, s19
	s_nop 0
	global_load_lds_dwordx4 v24, s[40:41]
	v_mov_b32_e32 v24, v194
	s_add_u32 s40, s14, 0xc080
	s_addc_u32 s41, s15, 0
	s_add_i32 m0, s19, 0x2000
	s_nop 0
	global_load_lds_dwordx4 v24, s[40:41]
	v_mov_b32_e32 v24, v195
	s_mov_b32 m0, s56
	s_add_u32 s40, s34, 0x4080
	s_addc_u32 s41, s35, 0
	global_load_lds_dwordx4 v24, s[42:43] sc1
	v_mov_b32_e32 v24, v195
	s_mov_b32 m0, s57
	s_nop 0
	global_load_lds_dwordx4 v24, s[40:41] sc1
	s_waitcnt vmcnt(8)
	s_waitcnt lgkmcnt(0)
	s_barrier
	s_setprio 3
	s_waitcnt lgkmcnt(0)
	v_mfma_f32_16x16x128_f8f6f4 v[48:51], v[8:15], v[16:23], v[136:139]
	v_mfma_f32_16x16x128_f8f6f4 v[52:55], v[200:207], v[16:23], v[140:143]
	v_mfma_f32_16x16x128_f8f6f4 v[32:35], v[8:15], v[128:135], v[144:147]
	v_mfma_f32_16x16x128_f8f6f4 v[36:39], v[200:207], v[128:135], v[148:151]
	v_mfma_f32_16x16x128_f8f6f4 v[24:27], v[8:15], v[224:231], v[152:155]
	v_mfma_f32_16x16x128_f8f6f4 v[28:31], v[200:207], v[224:231], v[156:159]
	v_mfma_f32_16x16x128_f8f6f4 v[8:11], v[8:15], v[232:239], v[160:163]
	v_mfma_f32_16x16x128_f8f6f4 v[12:15], v[200:207], v[232:239], v[164:167]
	v_mfma_f32_16x16x128_f8f6f4 v[72:75], v[208:215], v[16:23], v[168:171]
	v_mfma_f32_16x16x128_f8f6f4 v[76:79], v[216:223], v[16:23], v[172:175]
	v_mfma_f32_16x16x128_f8f6f4 v[40:43], v[208:215], v[128:135], v[176:179]
	v_mfma_f32_16x16x128_f8f6f4 v[44:47], v[216:223], v[128:135], v[180:183]
	v_mfma_f32_16x16x128_f8f6f4 v[16:19], v[208:215], v[224:231], v[184:187]
	v_mfma_f32_16x16x128_f8f6f4 v[20:23], v[216:223], v[224:231], v[188:191]
	v_mfma_f32_16x16x128_f8f6f4 v[0:3], v[208:215], v[232:239], v[0:3]
	v_mfma_f32_16x16x128_f8f6f4 v[4:7], v[216:223], v[232:239], v[4:7]
	s_setprio 0
	s_barrier
	s_andn2_b64 vcc, exec, s[22:23]
	s_cbranch_vccnz .LBB0_2726
	s_barrier
